# P8 single-wave sections: router bias requested before the barrier, 1/rms and gate weights kept in registers instead of store+reload; P11/P12 reuse the expert tile table P10 left in LDS; P2 token prefe
# speedup vs baseline: 1.0056x; 1.0051x over previous
; __device__ __forceinline__ float bf_lo(unsigned w) { return __uint_as_float(w << 16); }
; __device__ __forceinline__ float bf_hi(unsigned w) { return __uint_as_float(w & 0xffff0000u); }
; __global__ void __launch_bounds__(512, 2) fwd_kernel(Params p) {
;     ...
;         for (int blk = vcu; blk < T / 64; blk += G) {
;             const int tt = wave & 1, kq = wave >> 1, j = lane & 31, hh = lane >> 5;
;             if (tid < 32) hist[tid] = 0;
;             {
;                 const bf16_t* xr = X1 + (size_t)(blk * 64 + tt * 32 + j) * DM + kq * 512 + hh * 4;
;                 const float* wr_ = WrT + (size_t)j * DM + kq * 512 + hh * 4;
;                 f32x16 acc = {}; float ss = 0.f;
;                 u32x2 xb[2][8]; f32x4 wb[2][8];
; #pragma unroll
;                 for (int i = 0; i < 8; ++i) { xb[0][i] = *(const u32x2*)(xr + i * 8); wb[0][i] = *(const f32x4*)(wr_ + i * 8); }
; #pragma unroll
;                 for (int ch = 0; ch < 8; ++ch) {
;                     if (ch + 1 < 8) {
; #pragma unroll
;                         for (int i = 0; i < 8; ++i) { xb[(ch + 1) & 1][i] = *(const u32x2*)(xr + (ch + 1) * 64 + i * 8); wb[(ch + 1) & 1][i] = *(const f32x4*)(wr_ + (ch + 1) * 64 + i * 8); } }
; #pragma unroll
;                     for (int i = 0; i < 8; ++i) { const u32x2 xp = xb[ch & 1][i]; const f32x4 xv = {bf_lo(xp.x), bf_hi(xp.x), bf_lo(xp.y), bf_hi(xp.y)}, wv = wb[ch & 1][i];
;                         acc = __builtin_amdgcn_mfma_f32_32x32x2f32(wv.x, xv.x, acc, 0, 0, 0); acc = __builtin_amdgcn_mfma_f32_32x32x2f32(wv.y, xv.y, acc, 0, 0, 0);
;                         acc = __builtin_amdgcn_mfma_f32_32x32x2f32(wv.z, xv.z, acc, 0, 0, 0); acc = __builtin_amdgcn_mfma_f32_32x32x2f32(wv.w, xv.w, acc, 0, 0, 0);
;                         ss += (xv.x * xv.x + xv.y * xv.y) + (xv.z * xv.z + xv.w * xv.w); }
.LBB0_982:
	s_and_saveexec_b64 s[10:11], s[4:5]
	ds_write_b32 v132, v87 offset:53760
	s_or_b64 exec, exec, s[10:11]
	s_lshl_b32 s10, s78, 6
	v_or_b32_e32 v0, s10, v133
	v_ashrrev_i32_e32 v1, 31, v0
	v_lshlrev_b64 v[0:1], 12, v[0:1]
	v_lshl_add_u64 v[98:99], v[88:89], 0, v[0:1]
	global_load_dwordx2 v[0:1], v[98:99], off
	global_load_dwordx4 v[140:143], v[90:91], off
	global_load_dwordx2 v[110:111], v[98:99], off offset:16
	global_load_dwordx4 v[144:147], v[90:91], off offset:32
	global_load_dwordx2 v[106:107], v[98:99], off offset:32
	global_load_dwordx4 v[64:67], v[90:91], off offset:64
	global_load_dwordx2 v[102:103], v[98:99], off offset:48
	global_load_dwordx4 v[56:59], v[90:91], off offset:96
	global_load_dwordx2 v[82:83], v[98:99], off offset:64
	global_load_dwordx4 v[48:51], v[90:91], off offset:128
	global_load_dwordx2 v[80:81], v[98:99], off offset:80
	global_load_dwordx4 v[40:43], v[90:91], off offset:160
	global_load_dwordx2 v[74:75], v[98:99], off offset:96
	global_load_dwordx4 v[32:35], v[90:91], off offset:192
	global_load_dwordx2 v[72:73], v[98:99], off offset:112
	global_load_dwordx4 v[24:27], v[90:91], off offset:224
	global_load_dwordx2 v[128:129], v[98:99], off offset:128
	global_load_dwordx4 v[76:79], v[90:91], off offset:256
	global_load_dwordx2 v[124:125], v[98:99], off offset:144
	global_load_dwordx4 v[68:71], v[90:91], off offset:288
	global_load_dwordx2 v[120:121], v[98:99], off offset:160
	global_load_dwordx4 v[60:63], v[90:91], off offset:320
	global_load_dwordx2 v[116:117], v[98:99], off offset:176
	global_load_dwordx4 v[52:55], v[90:91], off offset:352
	global_load_dwordx2 v[112:113], v[98:99], off offset:192
	global_load_dwordx4 v[44:47], v[90:91], off offset:384
	global_load_dwordx2 v[108:109], v[98:99], off offset:208
	global_load_dwordx4 v[36:39], v[90:91], off offset:416
	global_load_dwordx2 v[104:105], v[98:99], off offset:224
	global_load_dwordx4 v[28:31], v[90:91], off offset:448
	global_load_dwordx2 v[100:101], v[98:99], off offset:240
	global_load_dwordx4 v[20:23], v[90:91], off offset:480
	s_waitcnt vmcnt(31)
	v_lshlrev_b32_e32 v114, 16, v0
	v_and_b32_e32 v115, 0xffff0000, v0
	v_lshlrev_b32_e32 v118, 16, v1
	v_and_b32_e32 v119, 0xffff0000, v1
	s_waitcnt vmcnt(30)
	v_mfma_f32_32x32x2_f32 v[0:15], v140, v114, 0
	v_mfma_f32_32x32x2_f32 v[0:15], v141, v115, v[0:15]
	v_mul_f32_e32 v115, v115, v115
	v_fmac_f32_e32 v115, v114, v114
	v_mul_f32_e32 v114, v119, v119
	v_fmac_f32_e32 v114, v118, v118
	v_add_f32_e32 v114, v115, v114
	s_waitcnt vmcnt(29)
	v_lshlrev_b32_e32 v115, 16, v110
	v_and_b32_e32 v110, 0xffff0000, v110
	s_waitcnt vmcnt(15)
	v_lshlrev_b32_e32 v141, 16, v128
	v_and_b32_e32 v128, 0xffff0000, v128
	v_mfma_f32_32x32x2_f32 v[0:15], v142, v118, v[0:15]
	v_lshlrev_b32_e32 v118, 16, v111
	v_and_b32_e32 v111, 0xffff0000, v111
	v_lshlrev_b32_e32 v142, 16, v129
	v_and_b32_e32 v129, 0xffff0000, v129
	v_mfma_f32_32x32x2_f32 v[0:15], v143, v119, v[0:15]
	v_mfma_f32_32x32x2_f32 v[0:15], v144, v115, v[0:15]
	v_mfma_f32_32x32x2_f32 v[0:15], v145, v110, v[0:15]
	v_mul_f32_e32 v110, v110, v110
	v_fmac_f32_e32 v110, v115, v115
	v_mfma_f32_32x32x2_f32 v[0:15], v146, v118, v[0:15]
	v_mfma_f32_32x32x2_f32 v[0:15], v147, v111, v[0:15]
	v_mul_f32_e32 v111, v111, v111
	v_fmac_f32_e32 v111, v118, v118
	v_add_f32_e32 v110, v110, v111
	v_lshlrev_b32_e32 v111, 16, v106
	v_and_b32_e32 v106, 0xffff0000, v106
	v_add_f32_e32 v110, v114, v110
	v_lshlrev_b32_e32 v114, 16, v107
	v_and_b32_e32 v107, 0xffff0000, v107
	v_mfma_f32_32x32x2_f32 v[0:15], v64, v111, v[0:15]
	v_mul_f32_e32 v64, v106, v106
	v_fmac_f32_e32 v64, v111, v111
	v_mfma_f32_32x32x2_f32 v[0:15], v65, v106, v[0:15]
	v_mul_f32_e32 v65, v107, v107
	v_fmac_f32_e32 v65, v114, v114
	v_add_f32_e32 v64, v64, v65
	v_lshlrev_b32_e32 v65, 16, v102
	v_add_f32_e32 v64, v110, v64
	v_mfma_f32_32x32x2_f32 v[0:15], v66, v114, v[0:15]
	v_and_b32_e32 v66, 0xffff0000, v102
	v_and_b32_e32 v102, 0xffff0000, v103
	v_mfma_f32_32x32x2_f32 v[0:15], v67, v107, v[0:15]
	v_lshlrev_b32_e32 v67, 16, v103
	v_mfma_f32_32x32x2_f32 v[0:15], v56, v65, v[0:15]
	v_mul_f32_e32 v56, v66, v66
	v_fmac_f32_e32 v56, v65, v65
	v_mfma_f32_32x32x2_f32 v[0:15], v57, v66, v[0:15]
	v_mul_f32_e32 v57, v102, v102
	v_fmac_f32_e32 v57, v67, v67
	v_add_f32_e32 v56, v56, v57
	v_lshlrev_b32_e32 v57, 16, v82
	v_add_f32_e32 v56, v64, v56
	v_and_b32_e32 v64, 0xffff0000, v83
	v_mfma_f32_32x32x2_f32 v[0:15], v58, v67, v[0:15]
	v_and_b32_e32 v58, 0xffff0000, v82
	v_mfma_f32_32x32x2_f32 v[0:15], v59, v102, v[0:15]
	v_lshlrev_b32_e32 v59, 16, v83
	v_mfma_f32_32x32x2_f32 v[0:15], v48, v57, v[0:15]
	v_mul_f32_e32 v48, v58, v58
	v_fmac_f32_e32 v48, v57, v57
	v_mfma_f32_32x32x2_f32 v[0:15], v49, v58, v[0:15]
	v_mul_f32_e32 v49, v64, v64
	v_fmac_f32_e32 v49, v59, v59
	v_add_f32_e32 v48, v48, v49
	v_lshlrev_b32_e32 v49, 16, v80
	v_add_f32_e32 v48, v56, v48
	v_and_b32_e32 v56, 0xffff0000, v81
	v_mfma_f32_32x32x2_f32 v[0:15], v50, v59, v[0:15]
	v_and_b32_e32 v50, 0xffff0000, v80
	v_mfma_f32_32x32x2_f32 v[0:15], v51, v64, v[0:15]
	v_lshlrev_b32_e32 v51, 16, v81
	v_mfma_f32_32x32x2_f32 v[0:15], v40, v49, v[0:15]
	v_mul_f32_e32 v40, v50, v50
	v_fmac_f32_e32 v40, v49, v49
	v_mfma_f32_32x32x2_f32 v[0:15], v41, v50, v[0:15]
	v_mul_f32_e32 v41, v56, v56
	v_fmac_f32_e32 v41, v51, v51
	v_add_f32_e32 v40, v40, v41
	v_lshlrev_b32_e32 v41, 16, v74
	v_add_f32_e32 v40, v48, v40
	v_and_b32_e32 v48, 0xffff0000, v75
	v_mfma_f32_32x32x2_f32 v[0:15], v42, v51, v[0:15]
	v_and_b32_e32 v42, 0xffff0000, v74
	v_mfma_f32_32x32x2_f32 v[0:15], v43, v56, v[0:15]
	v_lshlrev_b32_e32 v43, 16, v75
	v_mfma_f32_32x32x2_f32 v[0:15], v32, v41, v[0:15]
	v_mul_f32_e32 v32, v42, v42
; __device__ __forceinline__ float bf_lo(unsigned w) { return __uint_as_float(w << 16); }
; __device__ __forceinline__ float bf_hi(unsigned w) { return __uint_as_float(w & 0xffff0000u); }
; __global__ void __launch_bounds__(512, 2) fwd_kernel(Params p) {
;     ...
; #pragma unroll
;                 for (int i = 0; i < 8; ++i) { xb[0][i] = *(const u32x2*)(xr + i * 8); wb[0][i] = *(const f32x4*)(wr_ + i * 8); }
; #pragma unroll
;                 for (int ch = 0; ch < 8; ++ch) {
;                     if (ch + 1 < 8) {
; #pragma unroll
;                         for (int i = 0; i < 8; ++i) { xb[(ch + 1) & 1][i] = *(const u32x2*)(xr + (ch + 1) * 64 + i * 8); wb[(ch + 1) & 1][i] = *(const f32x4*)(wr_ + (ch + 1) * 64 + i * 8); } }
; #pragma unroll
;                     for (int i = 0; i < 8; ++i) { const u32x2 xp = xb[ch & 1][i]; const f32x4 xv = {bf_lo(xp.x), bf_hi(xp.x), bf_lo(xp.y), bf_hi(xp.y)}, wv = wb[ch & 1][i];
;                         acc = __builtin_amdgcn_mfma_f32_32x32x2f32(wv.x, xv.x, acc, 0, 0, 0); acc = __builtin_amdgcn_mfma_f32_32x32x2f32(wv.y, xv.y, acc, 0, 0, 0);
;                         acc = __builtin_amdgcn_mfma_f32_32x32x2f32(wv.z, xv.z, acc, 0, 0, 0); acc = __builtin_amdgcn_mfma_f32_32x32x2f32(wv.w, xv.w, acc, 0, 0, 0);
;                         ss += (xv.x * xv.x + xv.y * xv.y) + (xv.z * xv.z + xv.w * xv.w); }
;                 }
	v_fmac_f32_e32 v32, v41, v41
	v_mfma_f32_32x32x2_f32 v[0:15], v33, v42, v[0:15]
	v_mul_f32_e32 v33, v48, v48
	v_fmac_f32_e32 v33, v43, v43
	v_add_f32_e32 v32, v32, v33
	v_lshlrev_b32_e32 v33, 16, v72
	v_add_f32_e32 v32, v40, v32
	v_and_b32_e32 v40, 0xffff0000, v73
	v_mfma_f32_32x32x2_f32 v[0:15], v34, v43, v[0:15]
	v_and_b32_e32 v34, 0xffff0000, v72
	v_mfma_f32_32x32x2_f32 v[0:15], v35, v48, v[0:15]
	v_lshlrev_b32_e32 v35, 16, v73
	v_mfma_f32_32x32x2_f32 v[0:15], v24, v33, v[0:15]
	v_mul_f32_e32 v24, v34, v34
	v_fmac_f32_e32 v24, v33, v33
	v_mfma_f32_32x32x2_f32 v[0:15], v25, v34, v[0:15]
	v_mul_f32_e32 v25, v40, v40
	v_fmac_f32_e32 v25, v35, v35
	v_add_f32_e32 v24, v24, v25
	v_add_f32_e32 v140, v32, v24
	v_mfma_f32_32x32x2_f32 v[0:15], v26, v35, v[0:15]
	v_mfma_f32_32x32x2_f32 v[0:15], v27, v40, v[0:15]
	global_load_dwordx2 v[130:131], v[98:99], off offset:256
	global_load_dwordx4 v[80:83], v[90:91], off offset:512
	global_load_dwordx2 v[126:127], v[98:99], off offset:272
	global_load_dwordx4 v[72:75], v[90:91], off offset:544
	global_load_dwordx2 v[122:123], v[98:99], off offset:288
	global_load_dwordx4 v[64:67], v[90:91], off offset:576
	global_load_dwordx2 v[118:119], v[98:99], off offset:304
	global_load_dwordx4 v[56:59], v[90:91], off offset:608
	global_load_dwordx2 v[114:115], v[98:99], off offset:320
	global_load_dwordx4 v[48:51], v[90:91], off offset:640
	global_load_dwordx2 v[110:111], v[98:99], off offset:336
	global_load_dwordx4 v[40:43], v[90:91], off offset:672
	global_load_dwordx2 v[106:107], v[98:99], off offset:352
	global_load_dwordx4 v[32:35], v[90:91], off offset:704
	global_load_dwordx2 v[102:103], v[98:99], off offset:368
	global_load_dwordx4 v[24:27], v[90:91], off offset:736
	s_waitcnt vmcnt(30)
	v_mfma_f32_32x32x2_f32 v[0:15], v76, v141, v[0:15]
	v_mul_f32_e32 v76, v128, v128
	v_fmac_f32_e32 v76, v141, v141
	s_waitcnt vmcnt(15)
	v_lshlrev_b32_e32 v141, 16, v130
	v_mfma_f32_32x32x2_f32 v[0:15], v77, v128, v[0:15]
	v_mul_f32_e32 v77, v129, v129
	v_fmac_f32_e32 v77, v142, v142
	v_add_f32_e32 v76, v76, v77
	v_lshlrev_b32_e32 v77, 16, v124
	v_add_f32_e32 v76, v140, v76
	v_and_b32_e32 v130, 0xffff0000, v130
	v_mfma_f32_32x32x2_f32 v[0:15], v78, v142, v[0:15]
	v_and_b32_e32 v78, 0xffff0000, v124
	v_and_b32_e32 v124, 0xffff0000, v125
	v_lshlrev_b32_e32 v142, 16, v131
	v_and_b32_e32 v131, 0xffff0000, v131
	v_mfma_f32_32x32x2_f32 v[0:15], v79, v129, v[0:15]
	v_lshlrev_b32_e32 v79, 16, v125
	v_mfma_f32_32x32x2_f32 v[0:15], v68, v77, v[0:15]
	v_mul_f32_e32 v68, v78, v78
	v_fmac_f32_e32 v68, v77, v77
	v_mfma_f32_32x32x2_f32 v[0:15], v69, v78, v[0:15]
	v_mul_f32_e32 v69, v124, v124
	v_fmac_f32_e32 v69, v79, v79
	v_add_f32_e32 v68, v68, v69
	v_lshlrev_b32_e32 v69, 16, v120
	v_add_f32_e32 v68, v76, v68
	v_and_b32_e32 v76, 0xffff0000, v121
	v_mfma_f32_32x32x2_f32 v[0:15], v70, v79, v[0:15]
	v_and_b32_e32 v70, 0xffff0000, v120
	v_mfma_f32_32x32x2_f32 v[0:15], v71, v124, v[0:15]
	v_lshlrev_b32_e32 v71, 16, v121
	v_mfma_f32_32x32x2_f32 v[0:15], v60, v69, v[0:15]
	v_mul_f32_e32 v60, v70, v70
	v_fmac_f32_e32 v60, v69, v69
	v_mfma_f32_32x32x2_f32 v[0:15], v61, v70, v[0:15]
	v_mul_f32_e32 v61, v76, v76
	v_fmac_f32_e32 v61, v71, v71
	v_add_f32_e32 v60, v60, v61
	v_lshlrev_b32_e32 v61, 16, v116
	v_add_f32_e32 v60, v68, v60
	v_and_b32_e32 v68, 0xffff0000, v117
	v_mfma_f32_32x32x2_f32 v[0:15], v62, v71, v[0:15]
	v_and_b32_e32 v62, 0xffff0000, v116
	v_mfma_f32_32x32x2_f32 v[0:15], v63, v76, v[0:15]
	v_lshlrev_b32_e32 v63, 16, v117
	v_mfma_f32_32x32x2_f32 v[0:15], v52, v61, v[0:15]
	v_mul_f32_e32 v52, v62, v62
	v_fmac_f32_e32 v52, v61, v61
	v_mfma_f32_32x32x2_f32 v[0:15], v53, v62, v[0:15]
	v_mul_f32_e32 v53, v68, v68
	v_fmac_f32_e32 v53, v63, v63
	v_add_f32_e32 v52, v52, v53
	v_lshlrev_b32_e32 v53, 16, v112
	v_add_f32_e32 v52, v60, v52
	v_and_b32_e32 v60, 0xffff0000, v113
	v_mfma_f32_32x32x2_f32 v[0:15], v54, v63, v[0:15]
	v_and_b32_e32 v54, 0xffff0000, v112
	v_mfma_f32_32x32x2_f32 v[0:15], v55, v68, v[0:15]
	v_lshlrev_b32_e32 v55, 16, v113
	v_mfma_f32_32x32x2_f32 v[0:15], v44, v53, v[0:15]
	v_mul_f32_e32 v44, v54, v54
	v_fmac_f32_e32 v44, v53, v53
	v_mfma_f32_32x32x2_f32 v[0:15], v45, v54, v[0:15]
	v_mul_f32_e32 v45, v60, v60
	v_fmac_f32_e32 v45, v55, v55
	v_add_f32_e32 v44, v44, v45
	v_lshlrev_b32_e32 v45, 16, v108
	v_add_f32_e32 v44, v52, v44
	v_and_b32_e32 v52, 0xffff0000, v109
	v_mfma_f32_32x32x2_f32 v[0:15], v46, v55, v[0:15]
	v_and_b32_e32 v46, 0xffff0000, v108
	v_mfma_f32_32x32x2_f32 v[0:15], v47, v60, v[0:15]
	v_lshlrev_b32_e32 v47, 16, v109
	v_mfma_f32_32x32x2_f32 v[0:15], v36, v45, v[0:15]
	v_mul_f32_e32 v36, v46, v46
	v_fmac_f32_e32 v36, v45, v45
	v_mfma_f32_32x32x2_f32 v[0:15], v37, v46, v[0:15]
	v_mul_f32_e32 v37, v52, v52
	v_fmac_f32_e32 v37, v47, v47
	v_add_f32_e32 v36, v36, v37
	v_lshlrev_b32_e32 v37, 16, v104
	v_add_f32_e32 v36, v44, v36
	v_and_b32_e32 v44, 0xffff0000, v105
	v_mfma_f32_32x32x2_f32 v[0:15], v38, v47, v[0:15]
	v_and_b32_e32 v38, 0xffff0000, v104
	v_mfma_f32_32x32x2_f32 v[0:15], v39, v52, v[0:15]
	v_lshlrev_b32_e32 v39, 16, v105
	v_mfma_f32_32x32x2_f32 v[0:15], v28, v37, v[0:15]
	v_mul_f32_e32 v28, v38, v38
	v_fmac_f32_e32 v28, v37, v37
	v_mfma_f32_32x32x2_f32 v[0:15], v29, v38, v[0:15]
	v_mul_f32_e32 v29, v44, v44
	v_fmac_f32_e32 v29, v39, v39
	v_add_f32_e32 v28, v28, v29
	v_lshlrev_b32_e32 v29, 16, v100
	v_add_f32_e32 v28, v36, v28
	v_and_b32_e32 v36, 0xffff0000, v101
	v_mfma_f32_32x32x2_f32 v[0:15], v30, v39, v[0:15]
	v_and_b32_e32 v30, 0xffff0000, v100
	v_mfma_f32_32x32x2_f32 v[0:15], v31, v44, v[0:15]
	v_lshlrev_b32_e32 v31, 16, v101
	v_mfma_f32_32x32x2_f32 v[0:15], v20, v29, v[0:15]
	v_mul_f32_e32 v20, v30, v30
	v_fmac_f32_e32 v20, v29, v29
	v_mfma_f32_32x32x2_f32 v[0:15], v21, v30, v[0:15]
	v_mul_f32_e32 v21, v36, v36
	v_fmac_f32_e32 v21, v31, v31
	v_add_f32_e32 v20, v20, v21
	v_add_f32_e32 v140, v28, v20
	v_mfma_f32_32x32x2_f32 v[0:15], v22, v31, v[0:15]
	v_mfma_f32_32x32x2_f32 v[0:15], v23, v36, v[0:15]
	global_load_dwordx2 v[128:129], v[98:99], off offset:384
	global_load_dwordx4 v[76:79], v[90:91], off offset:768
	global_load_dwordx2 v[124:125], v[98:99], off offset:400
	global_load_dwordx4 v[68:71], v[90:91], off offset:800
	global_load_dwordx2 v[120:121], v[98:99], off offset:416
	global_load_dwordx4 v[60:63], v[90:91], off offset:832
	global_load_dwordx2 v[116:117], v[98:99], off offset:432
	global_load_dwordx4 v[52:55], v[90:91], off offset:864
	global_load_dwordx2 v[112:113], v[98:99], off offset:448
	global_load_dwordx4 v[44:47], v[90:91], off offset:896
	global_load_dwordx2 v[108:109], v[98:99], off offset:464
	global_load_dwordx4 v[36:39], v[90:91], off offset:928
	global_load_dwordx2 v[104:105], v[98:99], off offset:480
	global_load_dwordx4 v[28:31], v[90:91], off offset:960
	global_load_dwordx2 v[100:101], v[98:99], off offset:496
	global_load_dwordx4 v[20:23], v[90:91], off offset:992
	s_waitcnt vmcnt(30)
; __device__ __forceinline__ float bf_lo(unsigned w) { return __uint_as_float(w << 16); }
; __device__ __forceinline__ float bf_hi(unsigned w) { return __uint_as_float(w & 0xffff0000u); }
; __global__ void __launch_bounds__(512, 2) fwd_kernel(Params p) {
;     ...
; #pragma unroll
;                 for (int i = 0; i < 8; ++i) { xb[0][i] = *(const u32x2*)(xr + i * 8); wb[0][i] = *(const f32x4*)(wr_ + i * 8); }
; #pragma unroll
;                 for (int ch = 0; ch < 8; ++ch) {
;                     if (ch + 1 < 8) {
; #pragma unroll
;                         for (int i = 0; i < 8; ++i) { xb[(ch + 1) & 1][i] = *(const u32x2*)(xr + (ch + 1) * 64 + i * 8); wb[(ch + 1) & 1][i] = *(const f32x4*)(wr_ + (ch + 1) * 64 + i * 8); } }
; #pragma unroll
;                     for (int i = 0; i < 8; ++i) { const u32x2 xp = xb[ch & 1][i]; const f32x4 xv = {bf_lo(xp.x), bf_hi(xp.x), bf_lo(xp.y), bf_hi(xp.y)}, wv = wb[ch & 1][i];
;                         acc = __builtin_amdgcn_mfma_f32_32x32x2f32(wv.x, xv.x, acc, 0, 0, 0); acc = __builtin_amdgcn_mfma_f32_32x32x2f32(wv.y, xv.y, acc, 0, 0, 0);
;                         acc = __builtin_amdgcn_mfma_f32_32x32x2f32(wv.z, xv.z, acc, 0, 0, 0); acc = __builtin_amdgcn_mfma_f32_32x32x2f32(wv.w, xv.w, acc, 0, 0, 0);
;                         ss += (xv.x * xv.x + xv.y * xv.y) + (xv.z * xv.z + xv.w * xv.w); }
;                 }
	v_mfma_f32_32x32x2_f32 v[0:15], v80, v141, v[0:15]
	v_mul_f32_e32 v80, v130, v130
	v_fmac_f32_e32 v80, v141, v141
	s_waitcnt vmcnt(15)
	v_lshlrev_b32_e32 v141, 16, v128
	v_mfma_f32_32x32x2_f32 v[0:15], v81, v130, v[0:15]
	v_mul_f32_e32 v81, v131, v131
	v_fmac_f32_e32 v81, v142, v142
	v_add_f32_e32 v80, v80, v81
	v_lshlrev_b32_e32 v81, 16, v126
	v_add_f32_e32 v80, v140, v80
	v_and_b32_e32 v128, 0xffff0000, v128
	v_mfma_f32_32x32x2_f32 v[0:15], v82, v142, v[0:15]
	v_and_b32_e32 v82, 0xffff0000, v126
	v_and_b32_e32 v126, 0xffff0000, v127
	v_lshlrev_b32_e32 v142, 16, v129
	v_and_b32_e32 v129, 0xffff0000, v129
	v_mfma_f32_32x32x2_f32 v[0:15], v83, v131, v[0:15]
	v_lshlrev_b32_e32 v83, 16, v127
	v_mfma_f32_32x32x2_f32 v[0:15], v72, v81, v[0:15]
	v_mul_f32_e32 v72, v82, v82
	v_fmac_f32_e32 v72, v81, v81
	v_mfma_f32_32x32x2_f32 v[0:15], v73, v82, v[0:15]
	v_mul_f32_e32 v73, v126, v126
	v_fmac_f32_e32 v73, v83, v83
	v_add_f32_e32 v72, v72, v73
	v_lshlrev_b32_e32 v73, 16, v122
	v_add_f32_e32 v72, v80, v72
	v_and_b32_e32 v80, 0xffff0000, v123
	v_mfma_f32_32x32x2_f32 v[0:15], v74, v83, v[0:15]
	v_and_b32_e32 v74, 0xffff0000, v122
	v_mfma_f32_32x32x2_f32 v[0:15], v75, v126, v[0:15]
	v_lshlrev_b32_e32 v75, 16, v123
	v_mfma_f32_32x32x2_f32 v[0:15], v64, v73, v[0:15]
	v_mul_f32_e32 v64, v74, v74
	v_fmac_f32_e32 v64, v73, v73
	v_mfma_f32_32x32x2_f32 v[0:15], v65, v74, v[0:15]
	v_mul_f32_e32 v65, v80, v80
	v_fmac_f32_e32 v65, v75, v75
	v_add_f32_e32 v64, v64, v65
	v_lshlrev_b32_e32 v65, 16, v118
	v_add_f32_e32 v64, v72, v64
	v_and_b32_e32 v72, 0xffff0000, v119
	v_mfma_f32_32x32x2_f32 v[0:15], v66, v75, v[0:15]
	v_and_b32_e32 v66, 0xffff0000, v118
	v_mfma_f32_32x32x2_f32 v[0:15], v67, v80, v[0:15]
	v_lshlrev_b32_e32 v67, 16, v119
	v_mfma_f32_32x32x2_f32 v[0:15], v56, v65, v[0:15]
	v_mul_f32_e32 v56, v66, v66
	v_fmac_f32_e32 v56, v65, v65
	v_mfma_f32_32x32x2_f32 v[0:15], v57, v66, v[0:15]
	v_mul_f32_e32 v57, v72, v72
	v_fmac_f32_e32 v57, v67, v67
	v_add_f32_e32 v56, v56, v57
	v_lshlrev_b32_e32 v57, 16, v114
	v_add_f32_e32 v56, v64, v56
	v_and_b32_e32 v64, 0xffff0000, v115
	v_mfma_f32_32x32x2_f32 v[0:15], v58, v67, v[0:15]
	v_and_b32_e32 v58, 0xffff0000, v114
	v_mfma_f32_32x32x2_f32 v[0:15], v59, v72, v[0:15]
	v_lshlrev_b32_e32 v59, 16, v115
	v_mfma_f32_32x32x2_f32 v[0:15], v48, v57, v[0:15]
	v_mul_f32_e32 v48, v58, v58
	v_fmac_f32_e32 v48, v57, v57
	v_mfma_f32_32x32x2_f32 v[0:15], v49, v58, v[0:15]
	v_mul_f32_e32 v49, v64, v64
	v_fmac_f32_e32 v49, v59, v59
	v_add_f32_e32 v48, v48, v49
	v_lshlrev_b32_e32 v49, 16, v110
	v_add_f32_e32 v48, v56, v48
	v_and_b32_e32 v56, 0xffff0000, v111
	v_mfma_f32_32x32x2_f32 v[0:15], v50, v59, v[0:15]
	v_and_b32_e32 v50, 0xffff0000, v110
	v_mfma_f32_32x32x2_f32 v[0:15], v51, v64, v[0:15]
	v_lshlrev_b32_e32 v51, 16, v111
	v_mfma_f32_32x32x2_f32 v[0:15], v40, v49, v[0:15]
	v_mul_f32_e32 v40, v50, v50
	v_fmac_f32_e32 v40, v49, v49
	v_mfma_f32_32x32x2_f32 v[0:15], v41, v50, v[0:15]
	v_mul_f32_e32 v41, v56, v56
	v_fmac_f32_e32 v41, v51, v51
	v_add_f32_e32 v40, v40, v41
	v_lshlrev_b32_e32 v41, 16, v106
	v_add_f32_e32 v40, v48, v40
	v_and_b32_e32 v48, 0xffff0000, v107
	v_mfma_f32_32x32x2_f32 v[0:15], v42, v51, v[0:15]
	v_and_b32_e32 v42, 0xffff0000, v106
	v_mfma_f32_32x32x2_f32 v[0:15], v43, v56, v[0:15]
	v_lshlrev_b32_e32 v43, 16, v107
	v_mfma_f32_32x32x2_f32 v[0:15], v32, v41, v[0:15]
	v_mul_f32_e32 v32, v42, v42
	v_fmac_f32_e32 v32, v41, v41
	v_mfma_f32_32x32x2_f32 v[0:15], v33, v42, v[0:15]
	v_mul_f32_e32 v33, v48, v48
	v_fmac_f32_e32 v33, v43, v43
	v_add_f32_e32 v32, v32, v33
	v_lshlrev_b32_e32 v33, 16, v102
	v_add_f32_e32 v32, v40, v32
	v_and_b32_e32 v40, 0xffff0000, v103
	v_mfma_f32_32x32x2_f32 v[0:15], v34, v43, v[0:15]
	v_and_b32_e32 v34, 0xffff0000, v102
	v_mfma_f32_32x32x2_f32 v[0:15], v35, v48, v[0:15]
	v_lshlrev_b32_e32 v35, 16, v103
	v_mfma_f32_32x32x2_f32 v[0:15], v24, v33, v[0:15]
	v_mul_f32_e32 v24, v34, v34
	v_fmac_f32_e32 v24, v33, v33
	v_mfma_f32_32x32x2_f32 v[0:15], v25, v34, v[0:15]
	v_mul_f32_e32 v25, v40, v40
	v_fmac_f32_e32 v25, v35, v35
	v_add_f32_e32 v24, v24, v25
	v_add_f32_e32 v140, v32, v24
	v_mfma_f32_32x32x2_f32 v[0:15], v26, v35, v[0:15]
	v_mfma_f32_32x32x2_f32 v[0:15], v27, v40, v[0:15]
	global_load_dwordx2 v[130:131], v[98:99], off offset:512
	global_load_dwordx4 v[80:83], v[90:91], off offset:1024
	global_load_dwordx2 v[126:127], v[98:99], off offset:528
	global_load_dwordx4 v[72:75], v[90:91], off offset:1056
	global_load_dwordx2 v[122:123], v[98:99], off offset:544
	global_load_dwordx4 v[64:67], v[90:91], off offset:1088
	global_load_dwordx2 v[118:119], v[98:99], off offset:560
	global_load_dwordx4 v[56:59], v[90:91], off offset:1120
	global_load_dwordx2 v[114:115], v[98:99], off offset:576
	global_load_dwordx4 v[48:51], v[90:91], off offset:1152
	global_load_dwordx2 v[110:111], v[98:99], off offset:592
	global_load_dwordx4 v[40:43], v[90:91], off offset:1184
	global_load_dwordx2 v[106:107], v[98:99], off offset:608
	global_load_dwordx4 v[32:35], v[90:91], off offset:1216
	global_load_dwordx2 v[102:103], v[98:99], off offset:624
	global_load_dwordx4 v[24:27], v[90:91], off offset:1248
	s_waitcnt vmcnt(30)
	v_mfma_f32_32x32x2_f32 v[0:15], v76, v141, v[0:15]
	v_mul_f32_e32 v76, v128, v128
	v_fmac_f32_e32 v76, v141, v141
	s_waitcnt vmcnt(15)
; __device__ __forceinline__ float bf_lo(unsigned w) { return __uint_as_float(w << 16); }
; __device__ __forceinline__ float bf_hi(unsigned w) { return __uint_as_float(w & 0xffff0000u); }
; __global__ void __launch_bounds__(512, 2) fwd_kernel(Params p) {
;     ...
; #pragma unroll
;                 for (int i = 0; i < 8; ++i) { xb[0][i] = *(const u32x2*)(xr + i * 8); wb[0][i] = *(const f32x4*)(wr_ + i * 8); }
; #pragma unroll
;                 for (int ch = 0; ch < 8; ++ch) {
;                     if (ch + 1 < 8) {
; #pragma unroll
;                         for (int i = 0; i < 8; ++i) { xb[(ch + 1) & 1][i] = *(const u32x2*)(xr + (ch + 1) * 64 + i * 8); wb[(ch + 1) & 1][i] = *(const f32x4*)(wr_ + (ch + 1) * 64 + i * 8); } }
; #pragma unroll
;                     for (int i = 0; i < 8; ++i) { const u32x2 xp = xb[ch & 1][i]; const f32x4 xv = {bf_lo(xp.x), bf_hi(xp.x), bf_lo(xp.y), bf_hi(xp.y)}, wv = wb[ch & 1][i];
;                         acc = __builtin_amdgcn_mfma_f32_32x32x2f32(wv.x, xv.x, acc, 0, 0, 0); acc = __builtin_amdgcn_mfma_f32_32x32x2f32(wv.y, xv.y, acc, 0, 0, 0);
;                         acc = __builtin_amdgcn_mfma_f32_32x32x2f32(wv.z, xv.z, acc, 0, 0, 0); acc = __builtin_amdgcn_mfma_f32_32x32x2f32(wv.w, xv.w, acc, 0, 0, 0);
;                         ss += (xv.x * xv.x + xv.y * xv.y) + (xv.z * xv.z + xv.w * xv.w); }
;                 }
	v_lshlrev_b32_e32 v141, 16, v130
	v_mfma_f32_32x32x2_f32 v[0:15], v77, v128, v[0:15]
	v_mul_f32_e32 v77, v129, v129
	v_fmac_f32_e32 v77, v142, v142
	v_add_f32_e32 v76, v76, v77
	v_lshlrev_b32_e32 v77, 16, v124
	v_add_f32_e32 v76, v140, v76
	v_and_b32_e32 v130, 0xffff0000, v130
	v_mfma_f32_32x32x2_f32 v[0:15], v78, v142, v[0:15]
	v_and_b32_e32 v78, 0xffff0000, v124
	v_and_b32_e32 v124, 0xffff0000, v125
	v_lshlrev_b32_e32 v142, 16, v131
	v_and_b32_e32 v131, 0xffff0000, v131
	v_mfma_f32_32x32x2_f32 v[0:15], v79, v129, v[0:15]
	v_lshlrev_b32_e32 v79, 16, v125
	v_mfma_f32_32x32x2_f32 v[0:15], v68, v77, v[0:15]
	v_mul_f32_e32 v68, v78, v78
	v_fmac_f32_e32 v68, v77, v77
	v_mfma_f32_32x32x2_f32 v[0:15], v69, v78, v[0:15]
	v_mul_f32_e32 v69, v124, v124
	v_fmac_f32_e32 v69, v79, v79
	v_add_f32_e32 v68, v68, v69
	v_lshlrev_b32_e32 v69, 16, v120
	v_add_f32_e32 v68, v76, v68
	v_and_b32_e32 v76, 0xffff0000, v121
	v_mfma_f32_32x32x2_f32 v[0:15], v70, v79, v[0:15]
	v_and_b32_e32 v70, 0xffff0000, v120
	v_mfma_f32_32x32x2_f32 v[0:15], v71, v124, v[0:15]
	v_lshlrev_b32_e32 v71, 16, v121
	v_mfma_f32_32x32x2_f32 v[0:15], v60, v69, v[0:15]
	v_mul_f32_e32 v60, v70, v70
	v_fmac_f32_e32 v60, v69, v69
	v_mfma_f32_32x32x2_f32 v[0:15], v61, v70, v[0:15]
	v_mul_f32_e32 v61, v76, v76
	v_fmac_f32_e32 v61, v71, v71
	v_add_f32_e32 v60, v60, v61
	v_lshlrev_b32_e32 v61, 16, v116
	v_add_f32_e32 v60, v68, v60
	v_and_b32_e32 v68, 0xffff0000, v117
	v_mfma_f32_32x32x2_f32 v[0:15], v62, v71, v[0:15]
	v_and_b32_e32 v62, 0xffff0000, v116
	v_mfma_f32_32x32x2_f32 v[0:15], v63, v76, v[0:15]
	v_lshlrev_b32_e32 v63, 16, v117
	v_mfma_f32_32x32x2_f32 v[0:15], v52, v61, v[0:15]
	v_mul_f32_e32 v52, v62, v62
	v_fmac_f32_e32 v52, v61, v61
	v_mfma_f32_32x32x2_f32 v[0:15], v53, v62, v[0:15]
	v_mul_f32_e32 v53, v68, v68
	v_fmac_f32_e32 v53, v63, v63
	v_add_f32_e32 v52, v52, v53
	v_lshlrev_b32_e32 v53, 16, v112
	v_add_f32_e32 v52, v60, v52
	v_and_b32_e32 v60, 0xffff0000, v113
	v_mfma_f32_32x32x2_f32 v[0:15], v54, v63, v[0:15]
	v_and_b32_e32 v54, 0xffff0000, v112
	v_mfma_f32_32x32x2_f32 v[0:15], v55, v68, v[0:15]
	v_lshlrev_b32_e32 v55, 16, v113
	v_mfma_f32_32x32x2_f32 v[0:15], v44, v53, v[0:15]
	v_mul_f32_e32 v44, v54, v54
	v_fmac_f32_e32 v44, v53, v53
	v_mfma_f32_32x32x2_f32 v[0:15], v45, v54, v[0:15]
	v_mul_f32_e32 v45, v60, v60
	v_fmac_f32_e32 v45, v55, v55
	v_add_f32_e32 v44, v44, v45
	v_lshlrev_b32_e32 v45, 16, v108
	v_add_f32_e32 v44, v52, v44
	v_and_b32_e32 v52, 0xffff0000, v109
	v_mfma_f32_32x32x2_f32 v[0:15], v46, v55, v[0:15]
	v_and_b32_e32 v46, 0xffff0000, v108
	v_mfma_f32_32x32x2_f32 v[0:15], v47, v60, v[0:15]
	v_lshlrev_b32_e32 v47, 16, v109
	v_mfma_f32_32x32x2_f32 v[0:15], v36, v45, v[0:15]
	v_mul_f32_e32 v36, v46, v46
	v_fmac_f32_e32 v36, v45, v45
	v_mfma_f32_32x32x2_f32 v[0:15], v37, v46, v[0:15]
	v_mul_f32_e32 v37, v52, v52
	v_fmac_f32_e32 v37, v47, v47
	v_add_f32_e32 v36, v36, v37
	v_lshlrev_b32_e32 v37, 16, v104
	v_add_f32_e32 v36, v44, v36
	v_and_b32_e32 v44, 0xffff0000, v105
	v_mfma_f32_32x32x2_f32 v[0:15], v38, v47, v[0:15]
	v_and_b32_e32 v38, 0xffff0000, v104
	v_mfma_f32_32x32x2_f32 v[0:15], v39, v52, v[0:15]
	v_lshlrev_b32_e32 v39, 16, v105
	v_mfma_f32_32x32x2_f32 v[0:15], v28, v37, v[0:15]
	v_mul_f32_e32 v28, v38, v38
	v_fmac_f32_e32 v28, v37, v37
	v_mfma_f32_32x32x2_f32 v[0:15], v29, v38, v[0:15]
	v_mul_f32_e32 v29, v44, v44
	v_fmac_f32_e32 v29, v39, v39
	v_add_f32_e32 v28, v28, v29
	v_lshlrev_b32_e32 v29, 16, v100
	v_add_f32_e32 v28, v36, v28
	v_and_b32_e32 v36, 0xffff0000, v101
	v_mfma_f32_32x32x2_f32 v[0:15], v30, v39, v[0:15]
	v_and_b32_e32 v30, 0xffff0000, v100
	v_mfma_f32_32x32x2_f32 v[0:15], v31, v44, v[0:15]
	v_lshlrev_b32_e32 v31, 16, v101
	v_mfma_f32_32x32x2_f32 v[0:15], v20, v29, v[0:15]
	v_mul_f32_e32 v20, v30, v30
	v_fmac_f32_e32 v20, v29, v29
	v_mfma_f32_32x32x2_f32 v[0:15], v21, v30, v[0:15]
	v_mul_f32_e32 v21, v36, v36
	v_fmac_f32_e32 v21, v31, v31
	v_add_f32_e32 v20, v20, v21
	v_add_f32_e32 v140, v28, v20
	v_mfma_f32_32x32x2_f32 v[0:15], v22, v31, v[0:15]
	v_mfma_f32_32x32x2_f32 v[0:15], v23, v36, v[0:15]
	global_load_dwordx2 v[128:129], v[98:99], off offset:640
	global_load_dwordx4 v[76:79], v[90:91], off offset:1280
	global_load_dwordx2 v[124:125], v[98:99], off offset:656
	global_load_dwordx4 v[68:71], v[90:91], off offset:1312
	global_load_dwordx2 v[120:121], v[98:99], off offset:672
	global_load_dwordx4 v[60:63], v[90:91], off offset:1344
	global_load_dwordx2 v[116:117], v[98:99], off offset:688
	global_load_dwordx4 v[52:55], v[90:91], off offset:1376
	global_load_dwordx2 v[112:113], v[98:99], off offset:704
	global_load_dwordx4 v[44:47], v[90:91], off offset:1408
	global_load_dwordx2 v[108:109], v[98:99], off offset:720
	global_load_dwordx4 v[36:39], v[90:91], off offset:1440
	global_load_dwordx2 v[104:105], v[98:99], off offset:736
	global_load_dwordx4 v[28:31], v[90:91], off offset:1472
	global_load_dwordx2 v[100:101], v[98:99], off offset:752
	global_load_dwordx4 v[20:23], v[90:91], off offset:1504
	s_waitcnt vmcnt(30)
	v_mfma_f32_32x32x2_f32 v[0:15], v80, v141, v[0:15]
	v_mul_f32_e32 v80, v130, v130
	v_fmac_f32_e32 v80, v141, v141
	s_waitcnt vmcnt(15)
; __device__ __forceinline__ float bf_lo(unsigned w) { return __uint_as_float(w << 16); }
; __device__ __forceinline__ float bf_hi(unsigned w) { return __uint_as_float(w & 0xffff0000u); }
; __global__ void __launch_bounds__(512, 2) fwd_kernel(Params p) {
;     ...
; #pragma unroll
;                 for (int i = 0; i < 8; ++i) { xb[0][i] = *(const u32x2*)(xr + i * 8); wb[0][i] = *(const f32x4*)(wr_ + i * 8); }
; #pragma unroll
;                 for (int ch = 0; ch < 8; ++ch) {
;                     if (ch + 1 < 8) {
; #pragma unroll
;                         for (int i = 0; i < 8; ++i) { xb[(ch + 1) & 1][i] = *(const u32x2*)(xr + (ch + 1) * 64 + i * 8); wb[(ch + 1) & 1][i] = *(const f32x4*)(wr_ + (ch + 1) * 64 + i * 8); } }
; #pragma unroll
;                     for (int i = 0; i < 8; ++i) { const u32x2 xp = xb[ch & 1][i]; const f32x4 xv = {bf_lo(xp.x), bf_hi(xp.x), bf_lo(xp.y), bf_hi(xp.y)}, wv = wb[ch & 1][i];
;                         acc = __builtin_amdgcn_mfma_f32_32x32x2f32(wv.x, xv.x, acc, 0, 0, 0); acc = __builtin_amdgcn_mfma_f32_32x32x2f32(wv.y, xv.y, acc, 0, 0, 0);
;                         acc = __builtin_amdgcn_mfma_f32_32x32x2f32(wv.z, xv.z, acc, 0, 0, 0); acc = __builtin_amdgcn_mfma_f32_32x32x2f32(wv.w, xv.w, acc, 0, 0, 0);
;                         ss += (xv.x * xv.x + xv.y * xv.y) + (xv.z * xv.z + xv.w * xv.w); }
;                 }
	v_lshlrev_b32_e32 v141, 16, v128
	v_mfma_f32_32x32x2_f32 v[0:15], v81, v130, v[0:15]
	v_mul_f32_e32 v81, v131, v131
	v_fmac_f32_e32 v81, v142, v142
	v_add_f32_e32 v80, v80, v81
	v_lshlrev_b32_e32 v81, 16, v126
	v_add_f32_e32 v80, v140, v80
	v_and_b32_e32 v128, 0xffff0000, v128
	v_mfma_f32_32x32x2_f32 v[0:15], v82, v142, v[0:15]
	v_and_b32_e32 v82, 0xffff0000, v126
	v_and_b32_e32 v126, 0xffff0000, v127
	v_lshlrev_b32_e32 v142, 16, v129
	v_and_b32_e32 v129, 0xffff0000, v129
	v_mfma_f32_32x32x2_f32 v[0:15], v83, v131, v[0:15]
	v_lshlrev_b32_e32 v83, 16, v127
	v_mfma_f32_32x32x2_f32 v[0:15], v72, v81, v[0:15]
	v_mul_f32_e32 v72, v82, v82
	v_fmac_f32_e32 v72, v81, v81
	v_mfma_f32_32x32x2_f32 v[0:15], v73, v82, v[0:15]
	v_mul_f32_e32 v73, v126, v126
	v_fmac_f32_e32 v73, v83, v83
	v_add_f32_e32 v72, v72, v73
	v_lshlrev_b32_e32 v73, 16, v122
	v_add_f32_e32 v72, v80, v72
	v_and_b32_e32 v80, 0xffff0000, v123
	v_mfma_f32_32x32x2_f32 v[0:15], v74, v83, v[0:15]
	v_and_b32_e32 v74, 0xffff0000, v122
	v_mfma_f32_32x32x2_f32 v[0:15], v75, v126, v[0:15]
	v_lshlrev_b32_e32 v75, 16, v123
	v_mfma_f32_32x32x2_f32 v[0:15], v64, v73, v[0:15]
	v_mul_f32_e32 v64, v74, v74
	v_fmac_f32_e32 v64, v73, v73
	v_mfma_f32_32x32x2_f32 v[0:15], v65, v74, v[0:15]
	v_mul_f32_e32 v65, v80, v80
	v_fmac_f32_e32 v65, v75, v75
	v_add_f32_e32 v64, v64, v65
	v_lshlrev_b32_e32 v65, 16, v118
	v_add_f32_e32 v64, v72, v64
	v_and_b32_e32 v72, 0xffff0000, v119
	v_mfma_f32_32x32x2_f32 v[0:15], v66, v75, v[0:15]
	v_and_b32_e32 v66, 0xffff0000, v118
	v_mfma_f32_32x32x2_f32 v[0:15], v67, v80, v[0:15]
	v_lshlrev_b32_e32 v67, 16, v119
	v_mfma_f32_32x32x2_f32 v[0:15], v56, v65, v[0:15]
	v_mul_f32_e32 v56, v66, v66
	v_fmac_f32_e32 v56, v65, v65
	v_mfma_f32_32x32x2_f32 v[0:15], v57, v66, v[0:15]
	v_mul_f32_e32 v57, v72, v72
	v_fmac_f32_e32 v57, v67, v67
	v_add_f32_e32 v56, v56, v57
	v_lshlrev_b32_e32 v57, 16, v114
	v_add_f32_e32 v56, v64, v56
	v_and_b32_e32 v64, 0xffff0000, v115
	v_mfma_f32_32x32x2_f32 v[0:15], v58, v67, v[0:15]
	v_and_b32_e32 v58, 0xffff0000, v114
	v_mfma_f32_32x32x2_f32 v[0:15], v59, v72, v[0:15]
	v_lshlrev_b32_e32 v59, 16, v115
	v_mfma_f32_32x32x2_f32 v[0:15], v48, v57, v[0:15]
	v_mul_f32_e32 v48, v58, v58
	v_fmac_f32_e32 v48, v57, v57
	v_mfma_f32_32x32x2_f32 v[0:15], v49, v58, v[0:15]
	v_mul_f32_e32 v49, v64, v64
	v_fmac_f32_e32 v49, v59, v59
	v_add_f32_e32 v48, v48, v49
	v_lshlrev_b32_e32 v49, 16, v110
	v_add_f32_e32 v48, v56, v48
	v_and_b32_e32 v56, 0xffff0000, v111
	v_mfma_f32_32x32x2_f32 v[0:15], v50, v59, v[0:15]
	v_and_b32_e32 v50, 0xffff0000, v110
	v_mfma_f32_32x32x2_f32 v[0:15], v51, v64, v[0:15]
	v_lshlrev_b32_e32 v51, 16, v111
	v_mfma_f32_32x32x2_f32 v[0:15], v40, v49, v[0:15]
	v_mul_f32_e32 v40, v50, v50
	v_fmac_f32_e32 v40, v49, v49
	v_mfma_f32_32x32x2_f32 v[0:15], v41, v50, v[0:15]
	v_mul_f32_e32 v41, v56, v56
	v_fmac_f32_e32 v41, v51, v51
	v_add_f32_e32 v40, v40, v41
	v_lshlrev_b32_e32 v41, 16, v106
	v_add_f32_e32 v40, v48, v40
	v_and_b32_e32 v48, 0xffff0000, v107
	v_mfma_f32_32x32x2_f32 v[0:15], v42, v51, v[0:15]
	v_and_b32_e32 v42, 0xffff0000, v106
	v_mfma_f32_32x32x2_f32 v[0:15], v43, v56, v[0:15]
	v_lshlrev_b32_e32 v43, 16, v107
	v_mfma_f32_32x32x2_f32 v[0:15], v32, v41, v[0:15]
	v_mul_f32_e32 v32, v42, v42
	v_fmac_f32_e32 v32, v41, v41
	v_mfma_f32_32x32x2_f32 v[0:15], v33, v42, v[0:15]
	v_mul_f32_e32 v33, v48, v48
	v_fmac_f32_e32 v33, v43, v43
	v_add_f32_e32 v32, v32, v33
	v_lshlrev_b32_e32 v33, 16, v102
	v_add_f32_e32 v32, v40, v32
	v_and_b32_e32 v40, 0xffff0000, v103
	v_mfma_f32_32x32x2_f32 v[0:15], v34, v43, v[0:15]
	v_and_b32_e32 v34, 0xffff0000, v102
	v_mfma_f32_32x32x2_f32 v[0:15], v35, v48, v[0:15]
	v_lshlrev_b32_e32 v35, 16, v103
	v_mfma_f32_32x32x2_f32 v[0:15], v24, v33, v[0:15]
	v_mul_f32_e32 v24, v34, v34
	v_fmac_f32_e32 v24, v33, v33
	v_mfma_f32_32x32x2_f32 v[0:15], v25, v34, v[0:15]
	v_mul_f32_e32 v25, v40, v40
	v_fmac_f32_e32 v25, v35, v35
	v_add_f32_e32 v24, v24, v25
	v_add_f32_e32 v140, v32, v24
	v_mfma_f32_32x32x2_f32 v[0:15], v26, v35, v[0:15]
	v_mfma_f32_32x32x2_f32 v[0:15], v27, v40, v[0:15]
	global_load_dwordx2 v[130:131], v[98:99], off offset:768
	global_load_dwordx4 v[80:83], v[90:91], off offset:1536
	global_load_dwordx2 v[126:127], v[98:99], off offset:784
	global_load_dwordx4 v[72:75], v[90:91], off offset:1568
	global_load_dwordx2 v[122:123], v[98:99], off offset:800
	global_load_dwordx4 v[64:67], v[90:91], off offset:1600
	global_load_dwordx2 v[118:119], v[98:99], off offset:816
	global_load_dwordx4 v[56:59], v[90:91], off offset:1632
	global_load_dwordx2 v[114:115], v[98:99], off offset:832
	global_load_dwordx4 v[48:51], v[90:91], off offset:1664
	global_load_dwordx2 v[110:111], v[98:99], off offset:848
	global_load_dwordx4 v[40:43], v[90:91], off offset:1696
	global_load_dwordx2 v[106:107], v[98:99], off offset:864
	global_load_dwordx4 v[32:35], v[90:91], off offset:1728
	global_load_dwordx2 v[102:103], v[98:99], off offset:880
	global_load_dwordx4 v[24:27], v[90:91], off offset:1760
	s_waitcnt vmcnt(30)
	v_mfma_f32_32x32x2_f32 v[0:15], v76, v141, v[0:15]
	v_mul_f32_e32 v76, v128, v128
	v_fmac_f32_e32 v76, v141, v141
	v_mfma_f32_32x32x2_f32 v[0:15], v77, v128, v[0:15]
	v_mul_f32_e32 v77, v129, v129
	v_fmac_f32_e32 v77, v142, v142
	v_add_f32_e32 v76, v76, v77
	s_waitcnt vmcnt(29)
	v_lshlrev_b32_e32 v77, 16, v124
	v_add_f32_e32 v76, v140, v76
	s_waitcnt vmcnt(15)
; __device__ __forceinline__ float bf_lo(unsigned w) { return __uint_as_float(w << 16); }
; __device__ __forceinline__ float bf_hi(unsigned w) { return __uint_as_float(w & 0xffff0000u); }
; __global__ void __launch_bounds__(512, 2) fwd_kernel(Params p) {
;     ...
; #pragma unroll
;                 for (int i = 0; i < 8; ++i) { xb[0][i] = *(const u32x2*)(xr + i * 8); wb[0][i] = *(const f32x4*)(wr_ + i * 8); }
; #pragma unroll
;                 for (int ch = 0; ch < 8; ++ch) {
;                     if (ch + 1 < 8) {
; #pragma unroll
;                         for (int i = 0; i < 8; ++i) { xb[(ch + 1) & 1][i] = *(const u32x2*)(xr + (ch + 1) * 64 + i * 8); wb[(ch + 1) & 1][i] = *(const f32x4*)(wr_ + (ch + 1) * 64 + i * 8); } }
; #pragma unroll
;                     for (int i = 0; i < 8; ++i) { const u32x2 xp = xb[ch & 1][i]; const f32x4 xv = {bf_lo(xp.x), bf_hi(xp.x), bf_lo(xp.y), bf_hi(xp.y)}, wv = wb[ch & 1][i];
;                         acc = __builtin_amdgcn_mfma_f32_32x32x2f32(wv.x, xv.x, acc, 0, 0, 0); acc = __builtin_amdgcn_mfma_f32_32x32x2f32(wv.y, xv.y, acc, 0, 0, 0);
;                         acc = __builtin_amdgcn_mfma_f32_32x32x2f32(wv.z, xv.z, acc, 0, 0, 0); acc = __builtin_amdgcn_mfma_f32_32x32x2f32(wv.w, xv.w, acc, 0, 0, 0);
;                         ss += (xv.x * xv.x + xv.y * xv.y) + (xv.z * xv.z + xv.w * xv.w); }
;                 }
	v_lshlrev_b32_e32 v140, 16, v131
	v_mfma_f32_32x32x2_f32 v[0:15], v78, v142, v[0:15]
	v_and_b32_e32 v78, 0xffff0000, v124
	v_and_b32_e32 v124, 0xffff0000, v125
	v_and_b32_e32 v131, 0xffff0000, v131
	v_mfma_f32_32x32x2_f32 v[0:15], v79, v129, v[0:15]
	v_lshlrev_b32_e32 v79, 16, v125
	v_lshlrev_b32_e32 v129, 16, v130
	v_and_b32_e32 v130, 0xffff0000, v130
	v_mfma_f32_32x32x2_f32 v[0:15], v68, v77, v[0:15]
	v_mul_f32_e32 v68, v78, v78
	v_fmac_f32_e32 v68, v77, v77
	v_mfma_f32_32x32x2_f32 v[0:15], v69, v78, v[0:15]
	v_mul_f32_e32 v69, v124, v124
	v_fmac_f32_e32 v69, v79, v79
	v_add_f32_e32 v68, v68, v69
	v_lshlrev_b32_e32 v69, 16, v120
	v_add_f32_e32 v68, v76, v68
	v_and_b32_e32 v76, 0xffff0000, v121
	v_mfma_f32_32x32x2_f32 v[0:15], v70, v79, v[0:15]
	v_and_b32_e32 v70, 0xffff0000, v120
	v_mfma_f32_32x32x2_f32 v[0:15], v71, v124, v[0:15]
	v_lshlrev_b32_e32 v71, 16, v121
	v_mfma_f32_32x32x2_f32 v[0:15], v60, v69, v[0:15]
	v_mul_f32_e32 v60, v70, v70
	v_fmac_f32_e32 v60, v69, v69
	v_mfma_f32_32x32x2_f32 v[0:15], v61, v70, v[0:15]
	v_mul_f32_e32 v61, v76, v76
	v_fmac_f32_e32 v61, v71, v71
	v_add_f32_e32 v60, v60, v61
	v_lshlrev_b32_e32 v61, 16, v116
	v_add_f32_e32 v60, v68, v60
	v_and_b32_e32 v68, 0xffff0000, v117
	v_mfma_f32_32x32x2_f32 v[0:15], v62, v71, v[0:15]
	v_and_b32_e32 v62, 0xffff0000, v116
	v_mfma_f32_32x32x2_f32 v[0:15], v63, v76, v[0:15]
	v_lshlrev_b32_e32 v63, 16, v117
	v_mfma_f32_32x32x2_f32 v[0:15], v52, v61, v[0:15]
	v_mul_f32_e32 v52, v62, v62
	v_fmac_f32_e32 v52, v61, v61
	v_mfma_f32_32x32x2_f32 v[0:15], v53, v62, v[0:15]
	v_mul_f32_e32 v53, v68, v68
	v_fmac_f32_e32 v53, v63, v63
	v_add_f32_e32 v52, v52, v53
	v_lshlrev_b32_e32 v53, 16, v112
	v_add_f32_e32 v52, v60, v52
	v_and_b32_e32 v60, 0xffff0000, v113
	v_mfma_f32_32x32x2_f32 v[0:15], v54, v63, v[0:15]
	v_and_b32_e32 v54, 0xffff0000, v112
	v_mfma_f32_32x32x2_f32 v[0:15], v55, v68, v[0:15]
	v_lshlrev_b32_e32 v55, 16, v113
	v_mfma_f32_32x32x2_f32 v[0:15], v44, v53, v[0:15]
	v_mul_f32_e32 v44, v54, v54
	v_fmac_f32_e32 v44, v53, v53
	v_mfma_f32_32x32x2_f32 v[0:15], v45, v54, v[0:15]
	v_mul_f32_e32 v45, v60, v60
	v_fmac_f32_e32 v45, v55, v55
	v_add_f32_e32 v44, v44, v45
	v_lshlrev_b32_e32 v45, 16, v108
	v_add_f32_e32 v44, v52, v44
	v_and_b32_e32 v52, 0xffff0000, v109
	v_mfma_f32_32x32x2_f32 v[0:15], v46, v55, v[0:15]
	v_and_b32_e32 v46, 0xffff0000, v108
	v_mfma_f32_32x32x2_f32 v[0:15], v47, v60, v[0:15]
	v_lshlrev_b32_e32 v47, 16, v109
	v_mfma_f32_32x32x2_f32 v[0:15], v36, v45, v[0:15]
	v_mul_f32_e32 v36, v46, v46
	v_fmac_f32_e32 v36, v45, v45
	v_mfma_f32_32x32x2_f32 v[0:15], v37, v46, v[0:15]
	v_mul_f32_e32 v37, v52, v52
	v_fmac_f32_e32 v37, v47, v47
	v_add_f32_e32 v36, v36, v37
	v_lshlrev_b32_e32 v37, 16, v104
	v_add_f32_e32 v36, v44, v36
	v_and_b32_e32 v44, 0xffff0000, v105
	v_mfma_f32_32x32x2_f32 v[0:15], v38, v47, v[0:15]
	v_and_b32_e32 v38, 0xffff0000, v104
	v_mfma_f32_32x32x2_f32 v[0:15], v39, v52, v[0:15]
	v_lshlrev_b32_e32 v39, 16, v105
	v_mfma_f32_32x32x2_f32 v[0:15], v28, v37, v[0:15]
	v_mul_f32_e32 v28, v38, v38
	v_fmac_f32_e32 v28, v37, v37
	v_mfma_f32_32x32x2_f32 v[0:15], v29, v38, v[0:15]
	v_mul_f32_e32 v29, v44, v44
	v_fmac_f32_e32 v29, v39, v39
	v_add_f32_e32 v28, v28, v29
	v_lshlrev_b32_e32 v29, 16, v100
	v_add_f32_e32 v28, v36, v28
	v_and_b32_e32 v36, 0xffff0000, v101
	v_mfma_f32_32x32x2_f32 v[0:15], v30, v39, v[0:15]
	v_and_b32_e32 v30, 0xffff0000, v100
	v_mfma_f32_32x32x2_f32 v[0:15], v31, v44, v[0:15]
	v_lshlrev_b32_e32 v31, 16, v101
	v_mfma_f32_32x32x2_f32 v[0:15], v20, v29, v[0:15]
	v_mul_f32_e32 v20, v30, v30
	v_fmac_f32_e32 v20, v29, v29
	v_mfma_f32_32x32x2_f32 v[0:15], v21, v30, v[0:15]
	v_mul_f32_e32 v21, v36, v36
	v_fmac_f32_e32 v21, v31, v31
	v_add_f32_e32 v20, v20, v21
	v_add_f32_e32 v128, v28, v20
	v_mfma_f32_32x32x2_f32 v[0:15], v22, v31, v[0:15]
	v_mfma_f32_32x32x2_f32 v[0:15], v23, v36, v[0:15]
	global_load_dwordx2 v[124:125], v[98:99], off offset:896
	global_load_dwordx4 v[76:79], v[90:91], off offset:1792
	global_load_dwordx2 v[120:121], v[98:99], off offset:912
	global_load_dwordx4 v[68:71], v[90:91], off offset:1824
	global_load_dwordx2 v[116:117], v[98:99], off offset:928
	global_load_dwordx4 v[60:63], v[90:91], off offset:1856
	global_load_dwordx2 v[112:113], v[98:99], off offset:944
	global_load_dwordx4 v[52:55], v[90:91], off offset:1888
	global_load_dwordx2 v[108:109], v[98:99], off offset:960
	global_load_dwordx4 v[44:47], v[90:91], off offset:1920
	global_load_dwordx2 v[104:105], v[98:99], off offset:976
	global_load_dwordx4 v[36:39], v[90:91], off offset:1952
	global_load_dwordx2 v[100:101], v[98:99], off offset:992
	global_load_dwordx4 v[28:31], v[90:91], off offset:1984
	s_nop 0
	global_load_dwordx2 v[98:99], v[98:99], off offset:1008
	s_nop 0
	global_load_dwordx4 v[20:23], v[90:91], off offset:2016
	s_waitcnt vmcnt(30)
	v_mfma_f32_32x32x2_f32 v[0:15], v80, v129, v[0:15]
	s_waitcnt vmcnt(29)
	v_lshlrev_b32_e32 v80, 16, v126
	v_mfma_f32_32x32x2_f32 v[0:15], v81, v130, v[0:15]
	v_and_b32_e32 v81, 0xffff0000, v126
	v_mfma_f32_32x32x2_f32 v[0:15], v82, v140, v[0:15]
	v_lshlrev_b32_e32 v82, 16, v127
	v_mfma_f32_32x32x2_f32 v[0:15], v83, v131, v[0:15]
	v_and_b32_e32 v83, 0xffff0000, v127
	s_waitcnt vmcnt(28)
	v_mfma_f32_32x32x2_f32 v[0:15], v72, v80, v[0:15]
	s_waitcnt vmcnt(27)
	v_lshlrev_b32_e32 v72, 16, v122
	v_mfma_f32_32x32x2_f32 v[0:15], v73, v81, v[0:15]
	v_and_b32_e32 v73, 0xffff0000, v122
	v_mfma_f32_32x32x2_f32 v[0:15], v74, v82, v[0:15]
	v_lshlrev_b32_e32 v74, 16, v123
	v_mfma_f32_32x32x2_f32 v[0:15], v75, v83, v[0:15]
	v_and_b32_e32 v75, 0xffff0000, v123
	s_waitcnt vmcnt(26)
	v_mfma_f32_32x32x2_f32 v[0:15], v64, v72, v[0:15]
	s_waitcnt vmcnt(25)
; __device__ __forceinline__ float bf_lo(unsigned w) { return __uint_as_float(w << 16); }
; __device__ __forceinline__ float bf_hi(unsigned w) { return __uint_as_float(w & 0xffff0000u); }
; __global__ void __launch_bounds__(512, 2) fwd_kernel(Params p) {
;     ...
; #pragma unroll
;                 for (int i = 0; i < 8; ++i) { xb[0][i] = *(const u32x2*)(xr + i * 8); wb[0][i] = *(const f32x4*)(wr_ + i * 8); }
; #pragma unroll
;                 for (int ch = 0; ch < 8; ++ch) {
;                     if (ch + 1 < 8) {
; #pragma unroll
;                         for (int i = 0; i < 8; ++i) { xb[(ch + 1) & 1][i] = *(const u32x2*)(xr + (ch + 1) * 64 + i * 8); wb[(ch + 1) & 1][i] = *(const f32x4*)(wr_ + (ch + 1) * 64 + i * 8); } }
; #pragma unroll
;                     for (int i = 0; i < 8; ++i) { const u32x2 xp = xb[ch & 1][i]; const f32x4 xv = {bf_lo(xp.x), bf_hi(xp.x), bf_lo(xp.y), bf_hi(xp.y)}, wv = wb[ch & 1][i];
;                         acc = __builtin_amdgcn_mfma_f32_32x32x2f32(wv.x, xv.x, acc, 0, 0, 0); acc = __builtin_amdgcn_mfma_f32_32x32x2f32(wv.y, xv.y, acc, 0, 0, 0);
;                         acc = __builtin_amdgcn_mfma_f32_32x32x2f32(wv.z, xv.z, acc, 0, 0, 0); acc = __builtin_amdgcn_mfma_f32_32x32x2f32(wv.w, xv.w, acc, 0, 0, 0);
;                         ss += (xv.x * xv.x + xv.y * xv.y) + (xv.z * xv.z + xv.w * xv.w); }
;                 }
	v_lshlrev_b32_e32 v64, 16, v118
	v_mfma_f32_32x32x2_f32 v[0:15], v65, v73, v[0:15]
	v_and_b32_e32 v65, 0xffff0000, v118
	v_mfma_f32_32x32x2_f32 v[0:15], v66, v74, v[0:15]
	v_lshlrev_b32_e32 v66, 16, v119
	v_mfma_f32_32x32x2_f32 v[0:15], v67, v75, v[0:15]
	v_and_b32_e32 v67, 0xffff0000, v119
	s_waitcnt vmcnt(24)
	v_mfma_f32_32x32x2_f32 v[0:15], v56, v64, v[0:15]
	s_waitcnt vmcnt(23)
	v_lshlrev_b32_e32 v56, 16, v114
	v_mfma_f32_32x32x2_f32 v[0:15], v57, v65, v[0:15]
	v_and_b32_e32 v57, 0xffff0000, v114
	v_mfma_f32_32x32x2_f32 v[0:15], v58, v66, v[0:15]
	v_lshlrev_b32_e32 v58, 16, v115
	v_mfma_f32_32x32x2_f32 v[0:15], v59, v67, v[0:15]
	v_and_b32_e32 v59, 0xffff0000, v115
	s_waitcnt vmcnt(22)
	v_mfma_f32_32x32x2_f32 v[0:15], v48, v56, v[0:15]
	s_waitcnt vmcnt(21)
	v_lshlrev_b32_e32 v48, 16, v110
	v_mfma_f32_32x32x2_f32 v[0:15], v49, v57, v[0:15]
	v_and_b32_e32 v49, 0xffff0000, v110
	v_mfma_f32_32x32x2_f32 v[0:15], v50, v58, v[0:15]
	v_lshlrev_b32_e32 v50, 16, v111
	v_mfma_f32_32x32x2_f32 v[0:15], v51, v59, v[0:15]
	v_and_b32_e32 v51, 0xffff0000, v111
	s_waitcnt vmcnt(20)
	v_mfma_f32_32x32x2_f32 v[0:15], v40, v48, v[0:15]
	s_waitcnt vmcnt(19)
	v_lshlrev_b32_e32 v40, 16, v106
	v_mfma_f32_32x32x2_f32 v[0:15], v41, v49, v[0:15]
	v_and_b32_e32 v41, 0xffff0000, v106
	v_mfma_f32_32x32x2_f32 v[0:15], v42, v50, v[0:15]
	v_lshlrev_b32_e32 v42, 16, v107
	v_mfma_f32_32x32x2_f32 v[0:15], v43, v51, v[0:15]
	v_and_b32_e32 v43, 0xffff0000, v107
	s_waitcnt vmcnt(18)
	v_mfma_f32_32x32x2_f32 v[0:15], v32, v40, v[0:15]
	s_waitcnt vmcnt(17)
	v_lshlrev_b32_e32 v32, 16, v102
	v_mfma_f32_32x32x2_f32 v[0:15], v33, v41, v[0:15]
	v_and_b32_e32 v33, 0xffff0000, v102
	v_mfma_f32_32x32x2_f32 v[0:15], v34, v42, v[0:15]
	v_lshlrev_b32_e32 v34, 16, v103
	v_mfma_f32_32x32x2_f32 v[0:15], v35, v43, v[0:15]
	v_and_b32_e32 v35, 0xffff0000, v103
	s_waitcnt vmcnt(16)
	v_mfma_f32_32x32x2_f32 v[0:15], v24, v32, v[0:15]
	v_mul_f32_e32 v24, v130, v130
	v_fmac_f32_e32 v24, v129, v129
	v_mfma_f32_32x32x2_f32 v[0:15], v25, v33, v[0:15]
	v_mul_f32_e32 v25, v131, v131
	v_fmac_f32_e32 v25, v140, v140
	v_add_f32_e32 v24, v24, v25
	v_mul_f32_e32 v25, v81, v81
	v_fmac_f32_e32 v25, v80, v80
	v_add_f32_e32 v24, v128, v24
	v_mfma_f32_32x32x2_f32 v[0:15], v26, v34, v[0:15]
	v_mul_f32_e32 v26, v83, v83
	v_fmac_f32_e32 v26, v82, v82
	v_add_f32_e32 v25, v25, v26
	v_add_f32_e32 v24, v24, v25
	v_mul_f32_e32 v25, v73, v73
	v_mul_f32_e32 v26, v75, v75
	v_fmac_f32_e32 v25, v72, v72
	v_fmac_f32_e32 v26, v74, v74
	v_add_f32_e32 v25, v25, v26
	v_add_f32_e32 v24, v24, v25
	v_mul_f32_e32 v25, v65, v65
	v_mul_f32_e32 v26, v67, v67
	v_fmac_f32_e32 v25, v64, v64
	v_fmac_f32_e32 v26, v66, v66
	v_add_f32_e32 v25, v25, v26
	v_mfma_f32_32x32x2_f32 v[0:15], v27, v35, v[0:15]
	v_add_f32_e32 v24, v24, v25
	v_mul_f32_e32 v25, v57, v57
	v_mul_f32_e32 v26, v59, v59
	v_fmac_f32_e32 v25, v56, v56
	v_fmac_f32_e32 v26, v58, v58
	v_add_f32_e32 v25, v25, v26
	v_add_f32_e32 v24, v24, v25
	v_mul_f32_e32 v25, v49, v49
	v_mul_f32_e32 v26, v51, v51
	v_fmac_f32_e32 v25, v48, v48
	v_fmac_f32_e32 v26, v50, v50
	v_add_f32_e32 v25, v25, v26
	v_add_f32_e32 v24, v24, v25
	v_mul_f32_e32 v25, v41, v41
	v_mul_f32_e32 v26, v43, v43
	v_fmac_f32_e32 v25, v40, v40
	v_fmac_f32_e32 v26, v42, v42
	v_add_f32_e32 v25, v25, v26
	v_add_f32_e32 v24, v24, v25
	v_mul_f32_e32 v25, v33, v33
	v_mul_f32_e32 v26, v35, v35
	v_fmac_f32_e32 v25, v32, v32
	v_fmac_f32_e32 v26, v34, v34
	v_add_f32_e32 v25, v25, v26
	v_add_f32_e32 v24, v24, v25
	s_waitcnt vmcnt(15)
	v_lshlrev_b32_e32 v25, 16, v124
	v_and_b32_e32 v26, 0xffff0000, v124
	v_lshlrev_b32_e32 v27, 16, v125
	s_waitcnt vmcnt(14)
	v_mfma_f32_32x32x2_f32 v[0:15], v76, v25, v[0:15]
	v_and_b32_e32 v32, 0xffff0000, v125
	s_waitcnt vmcnt(13)
	v_and_b32_e32 v33, 0xffff0000, v121
	s_waitcnt vmcnt(11)
	v_and_b32_e32 v34, 0xffff0000, v117
	s_waitcnt vmcnt(9)
	v_and_b32_e32 v35, 0xffff0000, v113
	s_waitcnt vmcnt(7)
	v_and_b32_e32 v40, 0xffff0000, v109
	s_waitcnt vmcnt(5)
	v_and_b32_e32 v41, 0xffff0000, v105
	v_mfma_f32_32x32x2_f32 v[0:15], v77, v26, v[0:15]
	v_mul_f32_e32 v26, v26, v26
	v_fmac_f32_e32 v26, v25, v25
	v_mul_f32_e32 v25, v32, v32
	v_fmac_f32_e32 v25, v27, v27
	v_add_f32_e32 v25, v26, v25
	v_lshlrev_b32_e32 v26, 16, v120
	v_mfma_f32_32x32x2_f32 v[0:15], v78, v27, v[0:15]
	v_and_b32_e32 v27, 0xffff0000, v120
	v_mfma_f32_32x32x2_f32 v[0:15], v79, v32, v[0:15]
	v_lshlrev_b32_e32 v32, 16, v121
	v_mfma_f32_32x32x2_f32 v[0:15], v68, v26, v[0:15]
	v_mfma_f32_32x32x2_f32 v[0:15], v69, v27, v[0:15]
	v_mul_f32_e32 v27, v27, v27
	v_fmac_f32_e32 v27, v26, v26
	v_mul_f32_e32 v26, v33, v33
	v_fmac_f32_e32 v26, v32, v32
	v_add_f32_e32 v26, v27, v26
	v_lshlrev_b32_e32 v27, 16, v116
	v_mfma_f32_32x32x2_f32 v[0:15], v70, v32, v[0:15]
	v_and_b32_e32 v32, 0xffff0000, v116
	v_mfma_f32_32x32x2_f32 v[0:15], v71, v33, v[0:15]
	v_lshlrev_b32_e32 v33, 16, v117
	v_mfma_f32_32x32x2_f32 v[0:15], v60, v27, v[0:15]
	v_mfma_f32_32x32x2_f32 v[0:15], v61, v32, v[0:15]
	v_mul_f32_e32 v32, v32, v32
	v_fmac_f32_e32 v32, v27, v27
	v_mul_f32_e32 v27, v34, v34
	v_fmac_f32_e32 v27, v33, v33
	v_add_f32_e32 v27, v32, v27
	v_lshlrev_b32_e32 v32, 16, v112
	v_mfma_f32_32x32x2_f32 v[0:15], v62, v33, v[0:15]
	v_and_b32_e32 v33, 0xffff0000, v112
	v_mfma_f32_32x32x2_f32 v[0:15], v63, v34, v[0:15]
	v_lshlrev_b32_e32 v34, 16, v113
	v_mfma_f32_32x32x2_f32 v[0:15], v52, v32, v[0:15]
	v_mfma_f32_32x32x2_f32 v[0:15], v53, v33, v[0:15]
	v_mul_f32_e32 v33, v33, v33
	v_fmac_f32_e32 v33, v32, v32
	v_mul_f32_e32 v32, v35, v35
	v_fmac_f32_e32 v32, v34, v34
	v_add_f32_e32 v32, v33, v32
	v_lshlrev_b32_e32 v33, 16, v108
	v_mfma_f32_32x32x2_f32 v[0:15], v54, v34, v[0:15]
	v_and_b32_e32 v34, 0xffff0000, v108
	v_mfma_f32_32x32x2_f32 v[0:15], v55, v35, v[0:15]
	v_lshlrev_b32_e32 v35, 16, v109
	v_mfma_f32_32x32x2_f32 v[0:15], v44, v33, v[0:15]
	v_mfma_f32_32x32x2_f32 v[0:15], v45, v34, v[0:15]
	v_mul_f32_e32 v34, v34, v34
	v_fmac_f32_e32 v34, v33, v33
	v_mul_f32_e32 v33, v40, v40
	v_fmac_f32_e32 v33, v35, v35
	v_add_f32_e32 v33, v34, v33
	v_lshlrev_b32_e32 v34, 16, v104
	v_mfma_f32_32x32x2_f32 v[0:15], v46, v35, v[0:15]
	v_and_b32_e32 v35, 0xffff0000, v104
	v_mfma_f32_32x32x2_f32 v[0:15], v47, v40, v[0:15]
	v_lshlrev_b32_e32 v40, 16, v105
	s_waitcnt vmcnt(4)
; #define LAS __attribute__((address_space(3)))
; __global__ void __launch_bounds__(512, 2) fwd_kernel(Params p) {
;     ...
;                         acc = __builtin_amdgcn_mfma_f32_32x32x2f32(wv.x, xv.x, acc, 0, 0, 0); acc = __builtin_amdgcn_mfma_f32_32x32x2f32(wv.y, xv.y, acc, 0, 0, 0);
;                         acc = __builtin_amdgcn_mfma_f32_32x32x2f32(wv.z, xv.z, acc, 0, 0, 0); acc = __builtin_amdgcn_mfma_f32_32x32x2f32(wv.w, xv.w, acc, 0, 0, 0);
;                         ss += (xv.x * xv.x + xv.y * xv.y) + (xv.z * xv.z + xv.w * xv.w); }
;                 }
;                 LAS float* pp = part + ((kq * 2 + tt) * 32 + j) * 33;
; #pragma unroll
;                 for (int r = 0; r < 16; ++r) pp[(r & 3) + 8 * (r >> 2) + 4 * hh] = acc[r];
;                 ssq[((kq * 2 + tt) * 32 + j) * 2 + hh] = ss;
;             }
;             __syncthreads();
;             int te[4];
;             if (tid < 64) {
;                 const int t2 = tid >> 5, jj = tid & 31, tok = blk * 64 + tid;
;                 float s = 0.f;
; #pragma unroll
;                 for (int q = 0; q < 4; ++q) s += ssq[((q * 2 + t2) * 32 + jj) * 2] + ssq[((q * 2 + t2) * 32 + jj) * 2 + 1];
;                 const float rstd = rsqrtf(s * (1.f / DM) + RMS_EPS);
;                 RS2[tok] = rstd;
;                 float lgv[NE];
; #pragma unroll
;                 for (int e = 0; e < NE; ++e) { float v = 0.f;
; #pragma unroll
;                     for (int q = 0; q < 4; ++q) v += part[((q * 2 + t2) * 32 + jj) * 33 + e];
;                     lgv[e] = v * rstd + p.in[I_BR][e]; }
	v_mfma_f32_32x32x2_f32 v[0:15], v36, v34, v[0:15]
	s_waitcnt vmcnt(3)
	v_and_b32_e32 v36, 0xffff0000, v100
	v_mfma_f32_32x32x2_f32 v[0:15], v37, v35, v[0:15]
	v_mul_f32_e32 v35, v35, v35
	v_fmac_f32_e32 v35, v34, v34
	v_mul_f32_e32 v34, v41, v41
	v_fmac_f32_e32 v34, v40, v40
	v_add_f32_e32 v34, v35, v34
	v_lshlrev_b32_e32 v35, 16, v100
	v_lshlrev_b32_e32 v37, 16, v101
	v_mfma_f32_32x32x2_f32 v[0:15], v38, v40, v[0:15]
	v_and_b32_e32 v38, 0xffff0000, v101
	v_mfma_f32_32x32x2_f32 v[0:15], v39, v41, v[0:15]
	s_waitcnt vmcnt(2)
	v_mfma_f32_32x32x2_f32 v[0:15], v28, v35, v[0:15]
	v_mul_f32_e32 v28, v36, v36
	v_fmac_f32_e32 v28, v35, v35
	s_waitcnt vmcnt(1)
	v_and_b32_e32 v35, 0xffff0000, v99
	v_mfma_f32_32x32x2_f32 v[0:15], v29, v36, v[0:15]
	v_mul_f32_e32 v29, v38, v38
	v_fmac_f32_e32 v29, v37, v37
	v_add_f32_e32 v28, v28, v29
	v_lshlrev_b32_e32 v29, 16, v98
	v_mfma_f32_32x32x2_f32 v[0:15], v30, v37, v[0:15]
	v_and_b32_e32 v30, 0xffff0000, v98
	v_mfma_f32_32x32x2_f32 v[0:15], v31, v38, v[0:15]
	v_lshlrev_b32_e32 v31, 16, v99
	s_waitcnt vmcnt(0)
	v_mfma_f32_32x32x2_f32 v[0:15], v20, v29, v[0:15]
	v_mul_f32_e32 v20, v30, v30
	v_fmac_f32_e32 v20, v29, v29
	v_mfma_f32_32x32x2_f32 v[0:15], v21, v30, v[0:15]
	v_mul_f32_e32 v21, v35, v35
	v_fmac_f32_e32 v21, v31, v31
	v_add_f32_e32 v20, v20, v21
	v_mfma_f32_32x32x2_f32 v[0:15], v22, v31, v[0:15]
	v_mfma_f32_32x32x2_f32 v[0:15], v23, v35, v[0:15]
	s_nop 15
	s_nop 1
	ds_write2_b32 v85, v0, v1 offset1:1
	ds_write2_b32 v85, v2, v3 offset0:2 offset1:3
	ds_write2_b32 v85, v4, v5 offset0:8 offset1:9
	ds_write2_b32 v85, v6, v7 offset0:10 offset1:11
	ds_write2_b32 v85, v8, v9 offset0:16 offset1:17
	ds_write2_b32 v85, v10, v11 offset0:18 offset1:19
	ds_write2_b32 v85, v12, v13 offset0:24 offset1:25
	ds_write2_b32 v85, v14, v15 offset0:26 offset1:27
	v_add_f32_e32 v0, v24, v25
	v_add_f32_e32 v0, v0, v26
	v_add_f32_e32 v0, v0, v27
	v_add_f32_e32 v0, v0, v32
	v_add_f32_e32 v0, v0, v33
	v_add_f32_e32 v0, v0, v34
	v_add_f32_e32 v0, v0, v28
	v_add_u32_e32 v34, s10, v84
	v_add_f32_e32 v0, v0, v20
	v_ashrrev_i32_e32 v35, 31, v34
	ds_write_b32 v86, v0 offset:36864
	global_load_dwordx4 v[200:203], v87, s[38:39] offset:48
	global_load_dwordx4 v[204:207], v87, s[38:39] offset:32
	global_load_dwordx4 v[208:211], v87, s[38:39] offset:16
	global_load_dwordx4 v[212:215], v87, s[38:39]
	global_load_dwordx4 v[216:219], v87, s[38:39] offset:112
	global_load_dwordx4 v[220:223], v87, s[38:39] offset:96
	global_load_dwordx4 v[224:227], v87, s[38:39] offset:80
	global_load_dwordx4 v[228:231], v87, s[38:39] offset:64
	s_waitcnt lgkmcnt(0)
	s_barrier
	s_and_saveexec_b64 s[46:47], s[6:7]
	s_cbranch_execz .LBB0_986
	ds_read2st64_b64 v[0:3], v136 offset0:72 offset1:73
	ds_read2_b32 v[18:19], v135 offset1:1
	s_movk_i32 s0, 0x80
	s_waitcnt lgkmcnt(1)
	v_mov_b32_e32 v4, v0
	v_mov_b32_e32 v5, v2
	v_mov_b32_e32 v2, v1
	v_pk_add_f32 v[0:1], v[4:5], v[2:3]
	s_nop 0
	v_add_f32_e32 v0, 0, v0
	v_add_f32_e32 v6, v0, v1
	ds_read2st64_b64 v[0:3], v136 offset0:74 offset1:75
	s_waitcnt lgkmcnt(0)
	v_mov_b32_e32 v4, v0
	v_mov_b32_e32 v5, v2
	v_mov_b32_e32 v2, v1
	v_pk_add_f32 v[0:1], v[4:5], v[2:3]
	s_nop 0
	v_add_f32_e32 v0, v6, v0
	v_add_f32_e32 v0, v0, v1
	v_fmamk_f32 v0, v0, 0x3a000000, v137
	v_cmp_gt_f32_e32 vcc, s57, v0
	v_mul_f32_e32 v1, 0x4b800000, v0
	s_nop 0
	v_cndmask_b32_e32 v0, v0, v1, vcc
	v_rsq_f32_e32 v0, v0
	s_nop 0
	v_mul_f32_e32 v1, 0x45800000, v0
	v_cndmask_b32_e32 v16, v0, v1, vcc
	v_mov_b32_e32 v244, v16
	v_lshl_add_u64 v[0:1], v[34:35], 2, s[44:45]
	global_store_dword v[0:1], v16, off
	v_add_u32_e32 v1, 0x2100, v135
	ds_read2_b32 v[20:21], v1 offset1:1
	v_add_u32_e32 v1, 0x4200, v135
	ds_read2_b32 v[22:23], v1 offset1:1
	v_add_u32_e32 v1, 0x6300, v135
	ds_read2_b32 v[24:25], v1 offset1:1
	v_add_f32_e32 v0, 0, v18
	s_waitcnt lgkmcnt(2)
	v_add_f32_e32 v0, v0, v20
	s_waitcnt lgkmcnt(1)
	v_add_f32_e32 v0, v0, v22
	s_waitcnt lgkmcnt(0)
	v_add_f32_e32 v17, v0, v24
	s_waitcnt vmcnt(1)
	v_mov_b32_e32 v0, v200
	v_mov_b32_e32 v1, v201
	v_mov_b32_e32 v2, v202
	v_mov_b32_e32 v3, v203
	v_mov_b32_e32 v4, v204
	v_mov_b32_e32 v5, v205
	v_mov_b32_e32 v6, v206
	v_mov_b32_e32 v7, v207
	v_mov_b32_e32 v8, v208
	v_mov_b32_e32 v9, v209
	v_mov_b32_e32 v10, v210
	v_mov_b32_e32 v11, v211
	v_mov_b32_e32 v12, v212
	v_mov_b32_e32 v13, v213
	v_mov_b32_e32 v14, v214
	v_mov_b32_e32 v15, v215
	v_fma_f32 v37, v16, v17, v12
	v_add_f32_e32 v12, 0, v19
	v_add_f32_e32 v12, v12, v21
	v_add_f32_e32 v12, v12, v23
	v_add_f32_e32 v12, v12, v25
	v_fma_f32 v36, v16, v12, v13
	ds_read2_b32 v[12:13], v135 offset0:2 offset1:3
	v_add_u32_e32 v17, 0x2108, v135
	ds_read2_b32 v[18:19], v17 offset1:1
	v_add_u32_e32 v17, 0x4208, v135
	ds_read2_b32 v[20:21], v17 offset1:1
	v_add_u32_e32 v17, 0x6308, v135
	ds_read2_b32 v[22:23], v17 offset1:1
	s_waitcnt lgkmcnt(3)
	v_add_f32_e32 v12, 0, v12
	s_waitcnt lgkmcnt(2)
	v_add_f32_e32 v12, v12, v18
	s_waitcnt lgkmcnt(1)
	v_add_f32_e32 v12, v12, v20
	v_add_u32_e32 v17, 0x2110, v135
	s_waitcnt lgkmcnt(0)
	v_add_f32_e32 v12, v12, v22
	v_fma_f32 v14, v16, v12, v14
	v_add_f32_e32 v12, 0, v13
	v_add_f32_e32 v12, v12, v19
	v_add_f32_e32 v12, v12, v21
	v_add_f32_e32 v12, v12, v23
	v_fmac_f32_e32 v15, v16, v12
	ds_read2_b32 v[12:13], v135 offset0:4 offset1:5
	ds_read2_b32 v[18:19], v17 offset1:1
	v_add_u32_e32 v17, 0x4210, v135
	ds_read2_b32 v[20:21], v17 offset1:1
	v_add_u32_e32 v17, 0x6310, v135
	ds_read2_b32 v[22:23], v17 offset1:1
	s_waitcnt lgkmcnt(3)
	v_add_f32_e32 v12, 0, v12
	s_waitcnt lgkmcnt(2)
	v_add_f32_e32 v12, v12, v18
	s_waitcnt lgkmcnt(1)
	v_add_f32_e32 v12, v12, v20
	v_cmp_lg_f32_e32 vcc, s58, v37
	s_waitcnt lgkmcnt(0)
; __global__ void __launch_bounds__(512, 2) fwd_kernel(Params p) {
;     ...
;                 float lgv[NE];
; #pragma unroll
;                 for (int e = 0; e < NE; ++e) { float v = 0.f;
; #pragma unroll
;                     for (int q = 0; q < 4; ++q) v += part[((q * 2 + t2) * 32 + jj) * 33 + e];
;                     lgv[e] = v * rstd + p.in[I_BR][e]; }
	v_add_f32_e32 v12, v12, v22
	v_fma_f32 v39, v16, v12, v8
	v_add_f32_e32 v8, 0, v13
	v_add_f32_e32 v8, v8, v19
	v_add_f32_e32 v8, v8, v21
	v_add_f32_e32 v8, v8, v23
	v_fma_f32 v38, v16, v8, v9
	ds_read2_b32 v[8:9], v135 offset0:6 offset1:7
	v_add_u32_e32 v12, 0x2118, v135
	ds_read2_b32 v[12:13], v12 offset1:1
	s_waitcnt lgkmcnt(1)
	v_add_f32_e32 v8, 0, v8
	s_waitcnt lgkmcnt(0)
	v_add_f32_e32 v8, v8, v12
	v_add_u32_e32 v12, 0x4218, v135
	ds_read2_b32 v[18:19], v12 offset1:1
	v_add_u32_e32 v12, 0x6318, v135
	ds_read2_b32 v[20:21], v12 offset1:1
	v_add_u32_e32 v12, 0x2120, v135
	s_waitcnt lgkmcnt(1)
	v_add_f32_e32 v8, v8, v18
	s_waitcnt lgkmcnt(0)
	v_add_f32_e32 v8, v8, v20
	v_fma_f32 v10, v16, v8, v10
	v_add_f32_e32 v8, 0, v9
	v_add_f32_e32 v8, v8, v13
	v_add_f32_e32 v8, v8, v19
	v_add_f32_e32 v8, v8, v21
	v_fmac_f32_e32 v11, v16, v8
	ds_read2_b32 v[8:9], v135 offset0:8 offset1:9
	ds_read2_b32 v[12:13], v12 offset1:1
	s_waitcnt lgkmcnt(1)
	v_add_f32_e32 v8, 0, v8
	s_waitcnt lgkmcnt(0)
	v_add_f32_e32 v8, v8, v12
	v_add_u32_e32 v12, 0x4220, v135
	ds_read2_b32 v[18:19], v12 offset1:1
	v_add_u32_e32 v12, 0x6320, v135
	ds_read2_b32 v[20:21], v12 offset1:1
	s_waitcnt lgkmcnt(1)
	v_add_f32_e32 v8, v8, v18
	s_waitcnt lgkmcnt(0)
	v_add_f32_e32 v8, v8, v20
	v_fma_f32 v41, v16, v8, v4
	v_add_f32_e32 v4, 0, v9
	v_add_f32_e32 v4, v4, v13
	v_add_f32_e32 v4, v4, v19
	v_add_f32_e32 v4, v4, v21
	v_fma_f32 v40, v16, v4, v5
	ds_read2_b32 v[4:5], v135 offset0:10 offset1:11
	v_add_u32_e32 v8, 0x2128, v135
	ds_read2_b32 v[8:9], v8 offset1:1
	s_waitcnt lgkmcnt(1)
	v_add_f32_e32 v4, 0, v4
	s_waitcnt lgkmcnt(0)
	v_add_f32_e32 v4, v4, v8
	v_add_u32_e32 v8, 0x4228, v135
	ds_read2_b32 v[12:13], v8 offset1:1
	v_add_u32_e32 v8, 0x6328, v135
	ds_read2_b32 v[18:19], v8 offset1:1
	v_add_u32_e32 v8, 0x2130, v135
	s_waitcnt lgkmcnt(1)
	v_add_f32_e32 v4, v4, v12
	s_waitcnt lgkmcnt(0)
	v_add_f32_e32 v4, v4, v18
	v_fma_f32 v6, v16, v4, v6
	v_add_f32_e32 v4, 0, v5
	v_add_f32_e32 v4, v4, v9
	v_add_f32_e32 v4, v4, v13
	v_add_f32_e32 v4, v4, v19
	v_fmac_f32_e32 v7, v16, v4
	ds_read2_b32 v[4:5], v135 offset0:12 offset1:13
	ds_read2_b32 v[8:9], v8 offset1:1
	s_waitcnt lgkmcnt(1)
	v_add_f32_e32 v4, 0, v4
	s_waitcnt lgkmcnt(0)
	v_add_f32_e32 v4, v4, v8
	v_add_u32_e32 v8, 0x4230, v135
	ds_read2_b32 v[12:13], v8 offset1:1
	v_add_u32_e32 v8, 0x6330, v135
	ds_read2_b32 v[18:19], v8 offset1:1
	s_waitcnt lgkmcnt(1)
	v_add_f32_e32 v4, v4, v12
	s_waitcnt lgkmcnt(0)
	v_add_f32_e32 v4, v4, v18
	v_fma_f32 v43, v16, v4, v0
	v_add_f32_e32 v0, 0, v5
	v_add_f32_e32 v0, v0, v9
	v_add_f32_e32 v0, v0, v13
	v_add_f32_e32 v0, v0, v19
	v_fma_f32 v42, v16, v0, v1
	ds_read2_b32 v[0:1], v135 offset0:14 offset1:15
	v_add_u32_e32 v4, 0x2138, v135
	ds_read2_b32 v[4:5], v4 offset1:1
	s_waitcnt lgkmcnt(1)
	v_add_f32_e32 v0, 0, v0
	s_waitcnt lgkmcnt(0)
	v_add_f32_e32 v0, v0, v4
	v_add_u32_e32 v4, 0x4238, v135
	ds_read2_b32 v[8:9], v4 offset1:1
	v_add_u32_e32 v4, 0x6338, v135
	ds_read2_b32 v[12:13], v4 offset1:1
	v_add_u32_e32 v4, 0x2140, v135
	s_waitcnt lgkmcnt(1)
	v_add_f32_e32 v0, v0, v8
	s_waitcnt lgkmcnt(0)
	v_add_f32_e32 v0, v0, v12
	v_fma_f32 v2, v16, v0, v2
	v_add_f32_e32 v0, 0, v1
	v_add_f32_e32 v0, v0, v5
	v_add_f32_e32 v0, v0, v9
	v_add_f32_e32 v0, v0, v13
	v_fmac_f32_e32 v3, v16, v0
	ds_read2_b32 v[0:1], v135 offset0:16 offset1:17
	ds_read2_b32 v[4:5], v4 offset1:1
	s_waitcnt lgkmcnt(1)
	v_add_f32_e32 v0, 0, v0
	s_waitcnt lgkmcnt(0)
	v_add_f32_e32 v0, v0, v4
	v_add_u32_e32 v4, 0x4240, v135
	ds_read2_b32 v[8:9], v4 offset1:1
	v_add_u32_e32 v4, 0x6340, v135
	ds_read2_b32 v[12:13], v4 offset1:1
	v_mov_b32_e32 v18, v216
	v_mov_b32_e32 v19, v217
	v_mov_b32_e32 v20, v218
	v_mov_b32_e32 v21, v219
	v_mov_b32_e32 v22, v220
	v_mov_b32_e32 v23, v221
	v_mov_b32_e32 v24, v222
	v_mov_b32_e32 v25, v223
	v_mov_b32_e32 v26, v224
	v_mov_b32_e32 v27, v225
	v_mov_b32_e32 v28, v226
	v_mov_b32_e32 v29, v227
	v_mov_b32_e32 v30, v228
	v_mov_b32_e32 v31, v229
	v_mov_b32_e32 v32, v230
	v_mov_b32_e32 v33, v231
	s_waitcnt lgkmcnt(1)
	v_add_f32_e32 v0, v0, v8
	s_waitcnt lgkmcnt(0)
	v_add_f32_e32 v0, v0, v12
	v_fma_f32 v4, v16, v0, v30
	v_add_f32_e32 v0, 0, v1
	v_add_f32_e32 v0, v0, v5
	v_add_f32_e32 v0, v0, v9
	ds_read2_b32 v[8:9], v135 offset0:18 offset1:19
	v_add_u32_e32 v5, 0x2148, v135
	v_add_f32_e32 v0, v0, v13
	ds_read2_b32 v[12:13], v5 offset1:1
	v_add_u32_e32 v5, 0x4248, v135
	v_fma_f32 v0, v16, v0, v31
	ds_read2_b32 v[30:31], v5 offset1:1
	v_add_u32_e32 v5, 0x6348, v135
	ds_read2_b32 v[44:45], v5 offset1:1
	s_waitcnt lgkmcnt(3)
	v_add_f32_e32 v1, 0, v8
	v_add_f32_e32 v5, 0, v9
	ds_read2_b32 v[8:9], v135 offset0:20 offset1:21
	s_waitcnt lgkmcnt(3)
	v_add_f32_e32 v5, v5, v13
	s_waitcnt lgkmcnt(2)
	v_add_f32_e32 v5, v5, v31
	s_waitcnt lgkmcnt(1)
	v_add_f32_e32 v5, v5, v45
	v_fmac_f32_e32 v33, v16, v5
	s_waitcnt lgkmcnt(0)
	v_add_f32_e32 v5, 0, v8
	v_add_u32_e32 v8, 0x2150, v135
	v_add_f32_e32 v1, v1, v12
	ds_read2_b32 v[12:13], v8 offset1:1
	v_add_u32_e32 v8, 0x4250, v135
	v_add_f32_e32 v1, v1, v30
	ds_read2_b32 v[30:31], v8 offset1:1
	v_add_u32_e32 v8, 0x6350, v135
	v_add_f32_e32 v1, v1, v44
	ds_read2_b32 v[44:45], v8 offset1:1
	s_waitcnt lgkmcnt(2)
	v_add_f32_e32 v5, v5, v12
	s_waitcnt lgkmcnt(1)
	v_add_f32_e32 v5, v5, v30
	v_fma_f32 v1, v16, v1, v32
	s_waitcnt lgkmcnt(0)
	v_add_f32_e32 v5, v5, v44
	v_fma_f32 v8, v16, v5, v26
	v_add_f32_e32 v5, 0, v9
	v_add_f32_e32 v5, v5, v13
	ds_read2_b32 v[12:13], v135 offset0:22 offset1:23
	v_add_f32_e32 v5, v5, v31
	v_add_f32_e32 v5, v5, v45
	v_fma_f32 v5, v16, v5, v27
	s_waitcnt lgkmcnt(0)
; __global__ void __launch_bounds__(512, 2) fwd_kernel(Params p) {
;     ...
;                 float lgv[NE];
; #pragma unroll
;                 for (int e = 0; e < NE; ++e) { float v = 0.f;
; #pragma unroll
;                     for (int q = 0; q < 4; ++q) v += part[((q * 2 + t2) * 32 + jj) * 33 + e];
;                     lgv[e] = v * rstd + p.in[I_BR][e]; }
;                 unsigned mask = 0u; float tv[4];
; #pragma unroll
;                 for (int k = 0; k < 4; ++k) { float best = -__builtin_inff(); int be = 0;
; #pragma unroll
;                     for (int e = 0; e < NE; ++e) { const bool take = !((mask >> e) & 1u) && lgv[e] > best; best = take ? lgv[e] : best; be = take ? e : be; }
;                     mask |= 1u << be; tv[k] = best; te[k] = be; }
	v_add_f32_e32 v9, 0, v12
	v_add_u32_e32 v12, 0x2158, v135
	ds_read2_b32 v[26:27], v12 offset1:1
	v_add_u32_e32 v12, 0x4258, v135
	ds_read2_b32 v[30:31], v12 offset1:1
	v_add_u32_e32 v12, 0x6358, v135
	ds_read2_b32 v[44:45], v12 offset1:1
	v_add_f32_e32 v12, 0, v13
	s_waitcnt lgkmcnt(2)
	v_add_f32_e32 v9, v9, v26
	v_add_f32_e32 v12, v12, v27
	ds_read2_b32 v[26:27], v135 offset0:24 offset1:25
	v_add_u32_e32 v13, 0x2160, v135
	s_waitcnt lgkmcnt(2)
	v_add_f32_e32 v9, v9, v30
	v_add_f32_e32 v12, v12, v31
	ds_read2_b32 v[30:31], v13 offset1:1
	v_add_u32_e32 v13, 0x4260, v135
	s_waitcnt lgkmcnt(2)
	v_add_f32_e32 v9, v9, v44
	v_add_f32_e32 v12, v12, v45
	ds_read2_b32 v[44:45], v13 offset1:1
	v_add_u32_e32 v13, 0x6360, v135
	ds_read2_b32 v[46:47], v13 offset1:1
	v_fmac_f32_e32 v29, v16, v12
	s_waitcnt lgkmcnt(3)
	v_add_f32_e32 v12, 0, v26
	s_waitcnt lgkmcnt(2)
	v_add_f32_e32 v12, v12, v30
	s_waitcnt lgkmcnt(1)
	v_add_f32_e32 v12, v12, v44
	s_waitcnt lgkmcnt(0)
	v_add_f32_e32 v12, v12, v46
	v_fma_f32 v13, v16, v12, v22
	v_add_f32_e32 v12, 0, v27
	v_add_f32_e32 v12, v12, v31
	v_add_f32_e32 v12, v12, v45
	v_add_f32_e32 v12, v12, v47
	v_fma_f32 v12, v16, v12, v23
	ds_read2_b32 v[22:23], v135 offset0:26 offset1:27
	v_fma_f32 v9, v16, v9, v28
	s_waitcnt lgkmcnt(0)
	v_add_f32_e32 v17, 0, v22
	v_add_u32_e32 v22, 0x2168, v135
	ds_read2_b32 v[26:27], v22 offset1:1
	v_add_u32_e32 v22, 0x4268, v135
	ds_read2_b32 v[30:31], v22 offset1:1
	v_add_u32_e32 v22, 0x6368, v135
	ds_read2_b32 v[44:45], v22 offset1:1
	s_waitcnt lgkmcnt(2)
	v_add_f32_e32 v17, v17, v26
	s_waitcnt lgkmcnt(1)
	v_add_f32_e32 v17, v17, v30
	s_waitcnt lgkmcnt(0)
	v_add_f32_e32 v17, v17, v44
	v_fma_f32 v22, v16, v17, v24
	v_add_f32_e32 v17, 0, v23
	v_add_f32_e32 v17, v17, v27
	ds_read2_b32 v[26:27], v135 offset0:28 offset1:29
	v_add_u32_e32 v23, 0x2170, v135
	v_add_f32_e32 v17, v17, v31
	ds_read2_b32 v[30:31], v23 offset1:1
	v_add_u32_e32 v23, 0x4270, v135
	v_add_f32_e32 v17, v17, v45
	ds_read2_b32 v[44:45], v23 offset1:1
	v_add_u32_e32 v23, 0x6370, v135
	ds_read2_b32 v[46:47], v23 offset1:1
	v_fmac_f32_e32 v25, v16, v17
	s_waitcnt lgkmcnt(3)
	v_add_f32_e32 v17, 0, v26
	s_waitcnt lgkmcnt(2)
	v_add_f32_e32 v17, v17, v30
	s_waitcnt lgkmcnt(1)
	v_add_f32_e32 v17, v17, v44
	s_waitcnt lgkmcnt(0)
	v_add_f32_e32 v17, v17, v46
	v_fma_f32 v23, v16, v17, v18
	v_add_f32_e32 v17, 0, v27
	ds_read2_b32 v[26:27], v135 offset0:30 offset1:31
	v_add_u32_e32 v18, 0x2178, v135
	v_add_f32_e32 v17, v17, v31
	ds_read2_b32 v[30:31], v18 offset1:1
	v_add_u32_e32 v18, 0x4278, v135
	v_add_f32_e32 v17, v17, v45
	ds_read2_b32 v[44:45], v18 offset1:1
	v_add_u32_e32 v18, 0x6378, v135
	v_add_f32_e32 v17, v17, v47
	ds_read2_b32 v[46:47], v18 offset1:1
	v_fma_f32 v19, v16, v17, v19
	s_waitcnt lgkmcnt(3)
	v_add_f32_e32 v17, 0, v26
	s_waitcnt lgkmcnt(2)
	v_add_f32_e32 v17, v17, v30
	s_waitcnt lgkmcnt(1)
	v_add_f32_e32 v17, v17, v44
	s_waitcnt lgkmcnt(0)
	v_add_f32_e32 v17, v17, v46
	v_fma_f32 v20, v16, v17, v20
	v_add_f32_e32 v17, 0, v27
	v_add_f32_e32 v17, v17, v31
	v_add_f32_e32 v17, v17, v45
	v_add_f32_e32 v17, v17, v47
	v_fmac_f32_e32 v21, v16, v17
	v_cndmask_b32_e32 v16, v139, v37, vcc
	v_cmp_gt_f32_e32 vcc, v36, v16
	s_nop 1
	v_cndmask_b32_e32 v16, v16, v36, vcc
	v_cndmask_b32_e64 v17, 0, 1, vcc
	v_cmp_gt_f32_e32 vcc, v14, v16
	s_nop 1
	v_cndmask_b32_e32 v16, v16, v14, vcc
	v_cndmask_b32_e64 v17, v17, 2, vcc
	v_cmp_gt_f32_e32 vcc, v15, v16
	s_nop 1
	v_cndmask_b32_e32 v16, v16, v15, vcc
	v_cndmask_b32_e64 v17, v17, 3, vcc
	v_cmp_gt_f32_e32 vcc, v39, v16
	s_nop 1
	v_cndmask_b32_e32 v16, v16, v39, vcc
	v_cndmask_b32_e64 v17, v17, 4, vcc
	v_cmp_gt_f32_e32 vcc, v38, v16
	s_nop 1
	v_cndmask_b32_e32 v16, v16, v38, vcc
	v_cndmask_b32_e64 v17, v17, 5, vcc
	v_cmp_gt_f32_e32 vcc, v10, v16
	s_nop 1
	v_cndmask_b32_e32 v16, v16, v10, vcc
	v_cndmask_b32_e64 v17, v17, 6, vcc
	v_cmp_gt_f32_e32 vcc, v11, v16
	s_nop 1
	v_cndmask_b32_e32 v16, v16, v11, vcc
	v_cndmask_b32_e64 v17, v17, 7, vcc
	v_cmp_gt_f32_e32 vcc, v41, v16
	s_nop 1
	v_cndmask_b32_e32 v16, v16, v41, vcc
	v_cndmask_b32_e64 v17, v17, 8, vcc
	v_cmp_gt_f32_e32 vcc, v40, v16
	s_nop 1
	v_cndmask_b32_e32 v16, v16, v40, vcc
	v_cndmask_b32_e64 v17, v17, 9, vcc
	v_cmp_gt_f32_e32 vcc, v6, v16
	s_nop 1
	v_cndmask_b32_e32 v16, v16, v6, vcc
	v_cndmask_b32_e64 v17, v17, 10, vcc
	v_cmp_gt_f32_e32 vcc, v7, v16
	s_nop 1
	v_cndmask_b32_e32 v16, v16, v7, vcc
	v_cndmask_b32_e64 v17, v17, 11, vcc
	v_cmp_gt_f32_e32 vcc, v43, v16
	s_nop 1
	v_cndmask_b32_e32 v16, v16, v43, vcc
	v_cndmask_b32_e64 v17, v17, 12, vcc
	v_cmp_gt_f32_e32 vcc, v42, v16
	s_nop 1
	v_cndmask_b32_e32 v16, v16, v42, vcc
	v_cndmask_b32_e64 v17, v17, 13, vcc
	v_cmp_gt_f32_e32 vcc, v2, v16
	s_nop 1
	v_cndmask_b32_e32 v16, v16, v2, vcc
	v_cndmask_b32_e64 v17, v17, 14, vcc
	v_cmp_gt_f32_e32 vcc, v3, v16
	s_nop 1
	v_cndmask_b32_e32 v16, v16, v3, vcc
	v_cndmask_b32_e64 v17, v17, 15, vcc
	v_cmp_gt_f32_e32 vcc, v4, v16
	s_nop 1
	v_cndmask_b32_e32 v16, v16, v4, vcc
	v_cndmask_b32_e64 v17, v17, 16, vcc
	v_cmp_gt_f32_e32 vcc, v0, v16
	s_nop 1
	v_cndmask_b32_e32 v16, v16, v0, vcc
	v_cndmask_b32_e64 v17, v17, 17, vcc
	v_cmp_gt_f32_e32 vcc, v1, v16
	s_nop 1
	v_cndmask_b32_e32 v16, v16, v1, vcc
	v_cndmask_b32_e64 v17, v17, 18, vcc
	v_cmp_gt_f32_e32 vcc, v33, v16
	s_nop 1
	v_cndmask_b32_e32 v16, v16, v33, vcc
	v_cndmask_b32_e64 v17, v17, 19, vcc
	v_cmp_gt_f32_e32 vcc, v8, v16
	s_nop 1
	v_cndmask_b32_e32 v16, v16, v8, vcc
	v_cndmask_b32_e64 v17, v17, 20, vcc
	v_cmp_gt_f32_e32 vcc, v5, v16
	s_nop 1
	v_cndmask_b32_e32 v16, v16, v5, vcc
	v_cndmask_b32_e64 v17, v17, 21, vcc
	v_cmp_gt_f32_e32 vcc, v9, v16
	s_nop 1
	v_cndmask_b32_e32 v16, v16, v9, vcc
; __global__ void __launch_bounds__(512, 2) fwd_kernel(Params p) {
;     ...
;                 unsigned mask = 0u; float tv[4];
; #pragma unroll
;                 for (int k = 0; k < 4; ++k) { float best = -__builtin_inff(); int be = 0;
; #pragma unroll
;                     for (int e = 0; e < NE; ++e) { const bool take = !((mask >> e) & 1u) && lgv[e] > best; best = take ? lgv[e] : best; be = take ? e : be; }
;                     mask |= 1u << be; tv[k] = best; te[k] = be; }
	v_cndmask_b32_e64 v17, v17, 22, vcc
	v_cmp_gt_f32_e32 vcc, v29, v16
	s_nop 1
	v_cndmask_b32_e32 v16, v16, v29, vcc
	v_cndmask_b32_e64 v17, v17, 23, vcc
	v_cmp_gt_f32_e32 vcc, v13, v16
	s_nop 1
	v_cndmask_b32_e32 v16, v16, v13, vcc
	v_cndmask_b32_e64 v17, v17, 24, vcc
	v_cmp_gt_f32_e32 vcc, v12, v16
	s_nop 1
	v_cndmask_b32_e32 v16, v16, v12, vcc
	v_cndmask_b32_e64 v17, v17, 25, vcc
	v_cmp_gt_f32_e32 vcc, v22, v16
	s_nop 1
	v_cndmask_b32_e32 v16, v16, v22, vcc
	v_cndmask_b32_e64 v17, v17, 26, vcc
	v_cmp_gt_f32_e32 vcc, v25, v16
	s_nop 1
	v_cndmask_b32_e32 v16, v16, v25, vcc
	v_cndmask_b32_e64 v17, v17, 27, vcc
	v_cmp_gt_f32_e32 vcc, v23, v16
	s_nop 1
	v_cndmask_b32_e32 v16, v16, v23, vcc
	v_cndmask_b32_e64 v17, v17, 28, vcc
	v_cmp_gt_f32_e32 vcc, v19, v16
	s_nop 1
	v_cndmask_b32_e32 v16, v16, v19, vcc
	v_cndmask_b32_e64 v17, v17, 29, vcc
	v_cmp_gt_f32_e32 vcc, v20, v16
	s_nop 1
	v_cndmask_b32_e32 v18, v16, v20, vcc
	v_cndmask_b32_e64 v17, v17, 30, vcc
	v_cmp_gt_f32_e32 vcc, v21, v18
	s_nop 1
	v_cndmask_b32_e64 v16, v17, 31, vcc
	v_cndmask_b32_e32 v24, v18, v21, vcc
	v_cmp_eq_u32_e64 s[10:11], 0, v16
	v_cmp_nlg_f32_e32 vcc, s58, v37
	v_lshlrev_b32_e64 v18, v16, 1
	s_or_b64 s[10:11], s[10:11], vcc
	v_cndmask_b32_e64 v17, v37, v139, s[10:11]
	v_and_b32_e32 v26, 2, v18
	v_cmp_eq_u32_e64 s[10:11], 0, v26
	v_cmp_gt_f32_e64 s[12:13], v36, v17
	s_and_b64 s[10:11], s[10:11], s[12:13]
	v_cndmask_b32_e64 v17, v17, v36, s[10:11]
	v_and_b32_e32 v27, 4, v18
	v_cndmask_b32_e64 v26, 0, 1, s[10:11]
	v_cmp_eq_u32_e64 s[10:11], 0, v27
	v_cmp_gt_f32_e64 s[12:13], v14, v17
	s_and_b64 s[10:11], s[10:11], s[12:13]
	v_cndmask_b32_e64 v17, v17, v14, s[10:11]
	v_and_b32_e32 v27, 8, v18
	v_cndmask_b32_e64 v26, v26, 2, s[10:11]
	v_cmp_eq_u32_e64 s[10:11], 0, v27
	v_cmp_gt_f32_e64 s[12:13], v15, v17
	s_and_b64 s[10:11], s[10:11], s[12:13]
	v_cndmask_b32_e64 v17, v17, v15, s[10:11]
	v_and_b32_e32 v27, 16, v18
	v_cndmask_b32_e64 v26, v26, 3, s[10:11]
	v_cmp_eq_u32_e64 s[10:11], 0, v27
	v_cmp_gt_f32_e64 s[12:13], v39, v17
	s_and_b64 s[10:11], s[10:11], s[12:13]
	v_cndmask_b32_e64 v17, v17, v39, s[10:11]
	v_and_b32_e32 v27, 32, v18
	v_cndmask_b32_e64 v26, v26, 4, s[10:11]
	v_cmp_eq_u32_e64 s[10:11], 0, v27
	v_cmp_gt_f32_e64 s[12:13], v38, v17
	s_and_b64 s[10:11], s[10:11], s[12:13]
	v_cndmask_b32_e64 v17, v17, v38, s[10:11]
	v_and_b32_e32 v27, 64, v18
	v_cndmask_b32_e64 v26, v26, 5, s[10:11]
	v_cmp_eq_u32_e64 s[10:11], 0, v27
	v_cmp_gt_f32_e64 s[12:13], v10, v17
	s_and_b64 s[10:11], s[10:11], s[12:13]
	v_cndmask_b32_e64 v17, v17, v10, s[10:11]
	v_and_b32_e32 v27, 0x80, v18
	v_cndmask_b32_e64 v26, v26, 6, s[10:11]
	v_cmp_eq_u32_e64 s[10:11], 0, v27
	v_cmp_gt_f32_e64 s[12:13], v11, v17
	s_and_b64 s[10:11], s[10:11], s[12:13]
	v_cndmask_b32_e64 v17, v17, v11, s[10:11]
	v_and_b32_e32 v27, 0x100, v18
	v_cndmask_b32_e64 v26, v26, 7, s[10:11]
	v_cmp_eq_u32_e64 s[10:11], 0, v27
	v_cmp_gt_f32_e64 s[12:13], v41, v17
	s_and_b64 s[10:11], s[10:11], s[12:13]
	v_cndmask_b32_e64 v17, v17, v41, s[10:11]
	v_and_b32_e32 v27, 0x200, v18
	v_cndmask_b32_e64 v26, v26, 8, s[10:11]
	v_cmp_eq_u32_e64 s[10:11], 0, v27
	v_cmp_gt_f32_e64 s[12:13], v40, v17
	s_and_b64 s[10:11], s[10:11], s[12:13]
	v_cndmask_b32_e64 v17, v17, v40, s[10:11]
	v_and_b32_e32 v27, 0x400, v18
	v_cndmask_b32_e64 v26, v26, 9, s[10:11]
	v_cmp_eq_u32_e64 s[10:11], 0, v27
	v_cmp_gt_f32_e64 s[12:13], v6, v17
	s_and_b64 s[10:11], s[10:11], s[12:13]
	v_cndmask_b32_e64 v17, v17, v6, s[10:11]
	v_and_b32_e32 v27, 0x800, v18
	v_cndmask_b32_e64 v26, v26, 10, s[10:11]
	v_cmp_eq_u32_e64 s[10:11], 0, v27
	v_cmp_gt_f32_e64 s[12:13], v7, v17
	s_and_b64 s[10:11], s[10:11], s[12:13]
	v_cndmask_b32_e64 v17, v17, v7, s[10:11]
	v_and_b32_e32 v27, 0x1000, v18
	v_cndmask_b32_e64 v26, v26, 11, s[10:11]
	v_cmp_eq_u32_e64 s[10:11], 0, v27
	v_cmp_gt_f32_e64 s[12:13], v43, v17
	s_and_b64 s[10:11], s[10:11], s[12:13]
	v_cndmask_b32_e64 v17, v17, v43, s[10:11]
	v_and_b32_e32 v27, 0x2000, v18
	v_cndmask_b32_e64 v26, v26, 12, s[10:11]
	v_cmp_eq_u32_e64 s[10:11], 0, v27
	v_cmp_gt_f32_e64 s[12:13], v42, v17
	s_and_b64 s[10:11], s[10:11], s[12:13]
	v_cndmask_b32_e64 v17, v17, v42, s[10:11]
	v_and_b32_e32 v27, 0x4000, v18
	v_cndmask_b32_e64 v26, v26, 13, s[10:11]
	v_cmp_eq_u32_e64 s[10:11], 0, v27
	v_cmp_gt_f32_e64 s[12:13], v2, v17
	s_and_b64 s[10:11], s[10:11], s[12:13]
	v_cndmask_b32_e64 v17, v17, v2, s[10:11]
	v_and_b32_e32 v27, 0x8000, v18
	v_cndmask_b32_e64 v26, v26, 14, s[10:11]
	v_cmp_eq_u32_e64 s[10:11], 0, v27
	v_cmp_gt_f32_e64 s[12:13], v3, v17
	s_and_b64 s[10:11], s[10:11], s[12:13]
	v_cndmask_b32_e64 v17, v17, v3, s[10:11]
	v_and_b32_e32 v27, 0x10000, v18
	v_cndmask_b32_e64 v26, v26, 15, s[10:11]
	v_cmp_eq_u32_e64 s[10:11], 0, v27
	v_cmp_gt_f32_e64 s[12:13], v4, v17
	s_and_b64 s[10:11], s[10:11], s[12:13]
	v_cndmask_b32_e64 v17, v17, v4, s[10:11]
	v_and_b32_e32 v27, 0x20000, v18
	v_cndmask_b32_e64 v26, v26, 16, s[10:11]
	v_cmp_eq_u32_e64 s[10:11], 0, v27
	v_cmp_gt_f32_e64 s[12:13], v0, v17
	s_and_b64 s[10:11], s[10:11], s[12:13]
	v_cndmask_b32_e64 v17, v17, v0, s[10:11]
	v_and_b32_e32 v27, 0x40000, v18
	v_cndmask_b32_e64 v26, v26, 17, s[10:11]
	v_cmp_eq_u32_e64 s[10:11], 0, v27
	v_cmp_gt_f32_e64 s[12:13], v1, v17
	s_and_b64 s[10:11], s[10:11], s[12:13]
	v_cndmask_b32_e64 v17, v17, v1, s[10:11]
	v_and_b32_e32 v27, 0x80000, v18
	v_cndmask_b32_e64 v26, v26, 18, s[10:11]
	v_cmp_eq_u32_e64 s[10:11], 0, v27
	v_cmp_gt_f32_e64 s[12:13], v33, v17
	s_and_b64 s[10:11], s[10:11], s[12:13]
	v_cndmask_b32_e64 v17, v17, v33, s[10:11]
	v_and_b32_e32 v27, 0x100000, v18
	v_cndmask_b32_e64 v26, v26, 19, s[10:11]
	v_cmp_eq_u32_e64 s[10:11], 0, v27
; __global__ void __launch_bounds__(512, 2) fwd_kernel(Params p) {
;     ...
;                 for (int k = 0; k < 4; ++k) { float best = -__builtin_inff(); int be = 0;
; #pragma unroll
;                     for (int e = 0; e < NE; ++e) { const bool take = !((mask >> e) & 1u) && lgv[e] > best; best = take ? lgv[e] : best; be = take ? e : be; }
;                     mask |= 1u << be; tv[k] = best; te[k] = be; }
	v_cmp_gt_f32_e64 s[12:13], v8, v17
	s_and_b64 s[10:11], s[10:11], s[12:13]
	v_cndmask_b32_e64 v17, v17, v8, s[10:11]
	v_and_b32_e32 v27, 0x200000, v18
	v_cndmask_b32_e64 v26, v26, 20, s[10:11]
	v_cmp_eq_u32_e64 s[10:11], 0, v27
	v_cmp_gt_f32_e64 s[12:13], v5, v17
	s_and_b64 s[10:11], s[10:11], s[12:13]
	v_cndmask_b32_e64 v17, v17, v5, s[10:11]
	v_and_b32_e32 v27, 0x400000, v18
	v_cndmask_b32_e64 v26, v26, 21, s[10:11]
	v_cmp_eq_u32_e64 s[10:11], 0, v27
	v_cmp_gt_f32_e64 s[12:13], v9, v17
	s_and_b64 s[10:11], s[10:11], s[12:13]
	v_cndmask_b32_e64 v17, v17, v9, s[10:11]
	v_and_b32_e32 v27, 0x800000, v18
	v_cndmask_b32_e64 v26, v26, 22, s[10:11]
	v_cmp_eq_u32_e64 s[10:11], 0, v27
	v_cmp_gt_f32_e64 s[12:13], v29, v17
	s_and_b64 s[10:11], s[10:11], s[12:13]
	v_cndmask_b32_e64 v17, v17, v29, s[10:11]
	v_and_b32_e32 v27, 0x1000000, v18
	v_cndmask_b32_e64 v26, v26, 23, s[10:11]
	v_cmp_eq_u32_e64 s[10:11], 0, v27
	v_cmp_gt_f32_e64 s[12:13], v13, v17
	s_and_b64 s[10:11], s[10:11], s[12:13]
	v_cndmask_b32_e64 v17, v17, v13, s[10:11]
	v_and_b32_e32 v27, 0x2000000, v18
	v_cndmask_b32_e64 v26, v26, 24, s[10:11]
	v_cmp_eq_u32_e64 s[10:11], 0, v27
	v_cmp_gt_f32_e64 s[12:13], v12, v17
	s_and_b64 s[10:11], s[10:11], s[12:13]
	v_cndmask_b32_e64 v17, v17, v12, s[10:11]
	v_and_b32_e32 v27, 0x4000000, v18
	v_cndmask_b32_e64 v26, v26, 25, s[10:11]
	v_cmp_eq_u32_e64 s[10:11], 0, v27
	v_cmp_gt_f32_e64 s[12:13], v22, v17
	s_and_b64 s[10:11], s[10:11], s[12:13]
	v_cndmask_b32_e64 v17, v17, v22, s[10:11]
	v_and_b32_e32 v27, 0x8000000, v18
	v_cndmask_b32_e64 v26, v26, 26, s[10:11]
	v_cmp_eq_u32_e64 s[10:11], 0, v27
	v_cmp_gt_f32_e64 s[12:13], v25, v17
	s_and_b64 s[10:11], s[10:11], s[12:13]
	v_cndmask_b32_e64 v17, v17, v25, s[10:11]
	v_and_b32_e32 v27, 0x10000000, v18
	v_cndmask_b32_e64 v26, v26, 27, s[10:11]
	v_cmp_eq_u32_e64 s[10:11], 0, v27
	v_cmp_gt_f32_e64 s[12:13], v23, v17
	s_and_b64 s[10:11], s[10:11], s[12:13]
	v_cndmask_b32_e64 v17, v17, v23, s[10:11]
	v_and_b32_e32 v27, 0x20000000, v18
	v_cndmask_b32_e64 v26, v26, 28, s[10:11]
	v_cmp_eq_u32_e64 s[10:11], 0, v27
	v_cmp_gt_f32_e64 s[12:13], v19, v17
	s_and_b64 s[10:11], s[10:11], s[12:13]
	v_cndmask_b32_e64 v17, v17, v19, s[10:11]
	v_and_b32_e32 v27, 2.0, v18
	v_cndmask_b32_e64 v26, v26, 29, s[10:11]
	v_cmp_eq_u32_e64 s[10:11], 0, v27
	v_cmp_gt_f32_e64 s[12:13], v20, v17
	s_and_b64 s[10:11], s[10:11], s[12:13]
	v_cndmask_b32_e64 v27, v17, v20, s[10:11]
	v_cndmask_b32_e64 v26, v26, 30, s[10:11]
	v_cmp_ne_u32_e64 s[10:11], 31, v16
	v_cmp_gt_f32_e64 s[12:13], v21, v27
	s_and_b64 s[10:11], s[10:11], s[12:13]
	v_cndmask_b32_e64 v17, v26, 31, s[10:11]
	v_cndmask_b32_e64 v26, v27, v21, s[10:11]
	v_lshl_or_b32 v27, 1, v17, v18
	v_and_b32_e32 v18, 1, v27
	v_cmp_eq_u32_e64 s[10:11], 1, v18
	s_or_b64 s[10:11], s[10:11], vcc
	v_and_b32_e32 v28, 2, v27
	v_cndmask_b32_e64 v18, v37, v139, s[10:11]
	v_cmp_eq_u32_e64 s[10:11], 0, v28
	v_cmp_gt_f32_e64 s[12:13], v36, v18
	s_and_b64 s[10:11], s[10:11], s[12:13]
	v_cndmask_b32_e64 v18, v18, v36, s[10:11]
	v_and_b32_e32 v30, 4, v27
	v_cndmask_b32_e64 v28, 0, 1, s[10:11]
	v_cmp_eq_u32_e64 s[10:11], 0, v30
	v_cmp_gt_f32_e64 s[12:13], v14, v18
	s_and_b64 s[10:11], s[10:11], s[12:13]
	v_cndmask_b32_e64 v18, v18, v14, s[10:11]
	v_and_b32_e32 v30, 8, v27
	v_cndmask_b32_e64 v28, v28, 2, s[10:11]
	v_cmp_eq_u32_e64 s[10:11], 0, v30
	v_cmp_gt_f32_e64 s[12:13], v15, v18
	s_and_b64 s[10:11], s[10:11], s[12:13]
	v_cndmask_b32_e64 v18, v18, v15, s[10:11]
	v_and_b32_e32 v30, 16, v27
	v_cndmask_b32_e64 v28, v28, 3, s[10:11]
	v_cmp_eq_u32_e64 s[10:11], 0, v30
	v_cmp_gt_f32_e64 s[12:13], v39, v18
	s_and_b64 s[10:11], s[10:11], s[12:13]
	v_cndmask_b32_e64 v18, v18, v39, s[10:11]
	v_and_b32_e32 v30, 32, v27
	v_cndmask_b32_e64 v28, v28, 4, s[10:11]
	v_cmp_eq_u32_e64 s[10:11], 0, v30
	v_cmp_gt_f32_e64 s[12:13], v38, v18
	s_and_b64 s[10:11], s[10:11], s[12:13]
	v_cndmask_b32_e64 v18, v18, v38, s[10:11]
	v_and_b32_e32 v30, 64, v27
	v_cndmask_b32_e64 v28, v28, 5, s[10:11]
	v_cmp_eq_u32_e64 s[10:11], 0, v30
	v_cmp_gt_f32_e64 s[12:13], v10, v18
	s_and_b64 s[10:11], s[10:11], s[12:13]
	v_cndmask_b32_e64 v18, v18, v10, s[10:11]
	v_and_b32_e32 v30, 0x80, v27
	v_cndmask_b32_e64 v28, v28, 6, s[10:11]
	v_cmp_eq_u32_e64 s[10:11], 0, v30
	v_cmp_gt_f32_e64 s[12:13], v11, v18
	s_and_b64 s[10:11], s[10:11], s[12:13]
	v_cndmask_b32_e64 v18, v18, v11, s[10:11]
	v_and_b32_e32 v30, 0x100, v27
	v_cndmask_b32_e64 v28, v28, 7, s[10:11]
	v_cmp_eq_u32_e64 s[10:11], 0, v30
	v_cmp_gt_f32_e64 s[12:13], v41, v18
	s_and_b64 s[10:11], s[10:11], s[12:13]
	v_cndmask_b32_e64 v18, v18, v41, s[10:11]
	v_and_b32_e32 v30, 0x200, v27
	v_cndmask_b32_e64 v28, v28, 8, s[10:11]
	v_cmp_eq_u32_e64 s[10:11], 0, v30
	v_cmp_gt_f32_e64 s[12:13], v40, v18
	s_and_b64 s[10:11], s[10:11], s[12:13]
	v_cndmask_b32_e64 v18, v18, v40, s[10:11]
	v_and_b32_e32 v30, 0x400, v27
	v_cndmask_b32_e64 v28, v28, 9, s[10:11]
	v_cmp_eq_u32_e64 s[10:11], 0, v30
	v_cmp_gt_f32_e64 s[12:13], v6, v18
	s_and_b64 s[10:11], s[10:11], s[12:13]
	v_cndmask_b32_e64 v18, v18, v6, s[10:11]
	v_and_b32_e32 v30, 0x800, v27
	v_cndmask_b32_e64 v28, v28, 10, s[10:11]
	v_cmp_eq_u32_e64 s[10:11], 0, v30
	v_cmp_gt_f32_e64 s[12:13], v7, v18
	s_and_b64 s[10:11], s[10:11], s[12:13]
	v_cndmask_b32_e64 v18, v18, v7, s[10:11]
	v_and_b32_e32 v30, 0x1000, v27
	v_cndmask_b32_e64 v28, v28, 11, s[10:11]
	v_cmp_eq_u32_e64 s[10:11], 0, v30
	v_cmp_gt_f32_e64 s[12:13], v43, v18
	s_and_b64 s[10:11], s[10:11], s[12:13]
	v_cndmask_b32_e64 v18, v18, v43, s[10:11]
	v_and_b32_e32 v30, 0x2000, v27
	v_cndmask_b32_e64 v28, v28, 12, s[10:11]
	v_cmp_eq_u32_e64 s[10:11], 0, v30
	v_cmp_gt_f32_e64 s[12:13], v42, v18
; __global__ void __launch_bounds__(512, 2) fwd_kernel(Params p) {
;     ...
;                 for (int k = 0; k < 4; ++k) { float best = -__builtin_inff(); int be = 0;
; #pragma unroll
;                     for (int e = 0; e < NE; ++e) { const bool take = !((mask >> e) & 1u) && lgv[e] > best; best = take ? lgv[e] : best; be = take ? e : be; }
;                     mask |= 1u << be; tv[k] = best; te[k] = be; }
	s_and_b64 s[10:11], s[10:11], s[12:13]
	v_cndmask_b32_e64 v18, v18, v42, s[10:11]
	v_and_b32_e32 v30, 0x4000, v27
	v_cndmask_b32_e64 v28, v28, 13, s[10:11]
	v_cmp_eq_u32_e64 s[10:11], 0, v30
	v_cmp_gt_f32_e64 s[12:13], v2, v18
	s_and_b64 s[10:11], s[10:11], s[12:13]
	v_cndmask_b32_e64 v18, v18, v2, s[10:11]
	v_and_b32_e32 v30, 0x8000, v27
	v_cndmask_b32_e64 v28, v28, 14, s[10:11]
	v_cmp_eq_u32_e64 s[10:11], 0, v30
	v_cmp_gt_f32_e64 s[12:13], v3, v18
	s_and_b64 s[10:11], s[10:11], s[12:13]
	v_cndmask_b32_e64 v18, v18, v3, s[10:11]
	v_and_b32_e32 v30, 0x10000, v27
	v_cndmask_b32_e64 v28, v28, 15, s[10:11]
	v_cmp_eq_u32_e64 s[10:11], 0, v30
	v_cmp_gt_f32_e64 s[12:13], v4, v18
	s_and_b64 s[10:11], s[10:11], s[12:13]
	v_cndmask_b32_e64 v18, v18, v4, s[10:11]
	v_and_b32_e32 v30, 0x20000, v27
	v_cndmask_b32_e64 v28, v28, 16, s[10:11]
	v_cmp_eq_u32_e64 s[10:11], 0, v30
	v_cmp_gt_f32_e64 s[12:13], v0, v18
	s_and_b64 s[10:11], s[10:11], s[12:13]
	v_cndmask_b32_e64 v18, v18, v0, s[10:11]
	v_and_b32_e32 v30, 0x40000, v27
	v_cndmask_b32_e64 v28, v28, 17, s[10:11]
	v_cmp_eq_u32_e64 s[10:11], 0, v30
	v_cmp_gt_f32_e64 s[12:13], v1, v18
	s_and_b64 s[10:11], s[10:11], s[12:13]
	v_cndmask_b32_e64 v18, v18, v1, s[10:11]
	v_and_b32_e32 v30, 0x80000, v27
	v_cndmask_b32_e64 v28, v28, 18, s[10:11]
	v_cmp_eq_u32_e64 s[10:11], 0, v30
	v_cmp_gt_f32_e64 s[12:13], v33, v18
	s_and_b64 s[10:11], s[10:11], s[12:13]
	v_cndmask_b32_e64 v18, v18, v33, s[10:11]
	v_and_b32_e32 v30, 0x100000, v27
	v_cndmask_b32_e64 v28, v28, 19, s[10:11]
	v_cmp_eq_u32_e64 s[10:11], 0, v30
	v_cmp_gt_f32_e64 s[12:13], v8, v18
	s_and_b64 s[10:11], s[10:11], s[12:13]
	v_cndmask_b32_e64 v18, v18, v8, s[10:11]
	v_and_b32_e32 v30, 0x200000, v27
	v_cndmask_b32_e64 v28, v28, 20, s[10:11]
	v_cmp_eq_u32_e64 s[10:11], 0, v30
	v_cmp_gt_f32_e64 s[12:13], v5, v18
	s_and_b64 s[10:11], s[10:11], s[12:13]
	v_cndmask_b32_e64 v18, v18, v5, s[10:11]
	v_and_b32_e32 v30, 0x400000, v27
	v_cndmask_b32_e64 v28, v28, 21, s[10:11]
	v_cmp_eq_u32_e64 s[10:11], 0, v30
	v_cmp_gt_f32_e64 s[12:13], v9, v18
	s_and_b64 s[10:11], s[10:11], s[12:13]
	v_cndmask_b32_e64 v18, v18, v9, s[10:11]
	v_and_b32_e32 v30, 0x800000, v27
	v_cndmask_b32_e64 v28, v28, 22, s[10:11]
	v_cmp_eq_u32_e64 s[10:11], 0, v30
	v_cmp_gt_f32_e64 s[12:13], v29, v18
	s_and_b64 s[10:11], s[10:11], s[12:13]
	v_cndmask_b32_e64 v18, v18, v29, s[10:11]
	v_and_b32_e32 v30, 0x1000000, v27
	v_cndmask_b32_e64 v28, v28, 23, s[10:11]
	v_cmp_eq_u32_e64 s[10:11], 0, v30
	v_cmp_gt_f32_e64 s[12:13], v13, v18
	s_and_b64 s[10:11], s[10:11], s[12:13]
	v_cndmask_b32_e64 v18, v18, v13, s[10:11]
	v_and_b32_e32 v30, 0x2000000, v27
	v_cndmask_b32_e64 v28, v28, 24, s[10:11]
	v_cmp_eq_u32_e64 s[10:11], 0, v30
	v_cmp_gt_f32_e64 s[12:13], v12, v18
	s_and_b64 s[10:11], s[10:11], s[12:13]
	v_cndmask_b32_e64 v18, v18, v12, s[10:11]
	v_and_b32_e32 v30, 0x4000000, v27
	v_cndmask_b32_e64 v28, v28, 25, s[10:11]
	v_cmp_eq_u32_e64 s[10:11], 0, v30
	v_cmp_gt_f32_e64 s[12:13], v22, v18
	s_and_b64 s[10:11], s[10:11], s[12:13]
	v_cndmask_b32_e64 v18, v18, v22, s[10:11]
	v_and_b32_e32 v30, 0x8000000, v27
	v_cndmask_b32_e64 v28, v28, 26, s[10:11]
	v_cmp_eq_u32_e64 s[10:11], 0, v30
	v_cmp_gt_f32_e64 s[12:13], v25, v18
	s_and_b64 s[10:11], s[10:11], s[12:13]
	v_cndmask_b32_e64 v18, v18, v25, s[10:11]
	v_and_b32_e32 v30, 0x10000000, v27
	v_cndmask_b32_e64 v28, v28, 27, s[10:11]
	v_cmp_eq_u32_e64 s[10:11], 0, v30
	v_cmp_gt_f32_e64 s[12:13], v23, v18
	s_and_b64 s[10:11], s[10:11], s[12:13]
	v_cndmask_b32_e64 v18, v18, v23, s[10:11]
	v_and_b32_e32 v30, 0x20000000, v27
	v_cndmask_b32_e64 v28, v28, 28, s[10:11]
	v_cmp_eq_u32_e64 s[10:11], 0, v30
	v_cmp_gt_f32_e64 s[12:13], v19, v18
	s_and_b64 s[10:11], s[10:11], s[12:13]
	v_cndmask_b32_e64 v18, v18, v19, s[10:11]
	v_and_b32_e32 v30, 2.0, v27
	v_cndmask_b32_e64 v28, v28, 29, s[10:11]
	v_cmp_eq_u32_e64 s[10:11], 0, v30
	v_cmp_gt_f32_e64 s[12:13], v20, v18
	s_and_b64 s[10:11], s[10:11], s[12:13]
	v_cndmask_b32_e64 v30, v18, v20, s[10:11]
	v_cndmask_b32_e64 v28, v28, 30, s[10:11]
	v_cmp_lt_i32_e64 s[10:11], -1, v27
	v_cmp_gt_f32_e64 s[12:13], v21, v30
	s_and_b64 s[10:11], s[10:11], s[12:13]
	v_cndmask_b32_e64 v18, v28, 31, s[10:11]
	v_cndmask_b32_e64 v28, v30, v21, s[10:11]
	v_lshlrev_b32_e64 v30, v18, 1
	v_or_b32_e32 v31, v30, v27
	v_and_b32_e32 v32, 1, v31
	v_cmp_eq_u32_e64 s[10:11], 1, v32
	s_or_b64 vcc, s[10:11], vcc
	v_cndmask_b32_e32 v32, v37, v139, vcc
	v_bitop3_b32 v37, v30, 2, v27 bitop3:0xc8
	v_cmp_eq_u32_e32 vcc, 0, v37
	v_cmp_gt_f32_e64 s[10:11], v36, v32
	s_and_b64 vcc, vcc, s[10:11]
	v_cndmask_b32_e32 v32, v32, v36, vcc
	v_bitop3_b32 v36, v30, 4, v27 bitop3:0xc8
	v_cndmask_b32_e64 v37, 0, 1, vcc
	v_cmp_eq_u32_e32 vcc, 0, v36
	v_cmp_gt_f32_e64 s[10:11], v14, v32
	s_and_b64 vcc, vcc, s[10:11]
	v_cndmask_b32_e32 v14, v32, v14, vcc
	v_bitop3_b32 v32, v30, 8, v27 bitop3:0xc8
	v_cndmask_b32_e64 v36, v37, 2, vcc
	v_cmp_eq_u32_e32 vcc, 0, v32
	v_cmp_gt_f32_e64 s[10:11], v15, v14
	s_and_b64 vcc, vcc, s[10:11]
	v_cndmask_b32_e32 v14, v14, v15, vcc
	v_bitop3_b32 v15, v30, 16, v27 bitop3:0xc8
	v_cndmask_b32_e64 v32, v36, 3, vcc
	v_cmp_eq_u32_e32 vcc, 0, v15
	v_cmp_gt_f32_e64 s[10:11], v39, v14
	s_and_b64 vcc, vcc, s[10:11]
	v_cndmask_b32_e64 v15, v32, 4, vcc
	v_cndmask_b32_e32 v14, v14, v39, vcc
	v_bitop3_b32 v32, v30, 32, v27 bitop3:0xc8
	v_cmp_eq_u32_e32 vcc, 0, v32
	v_cmp_gt_f32_e64 s[10:11], v38, v14
	s_and_b64 vcc, vcc, s[10:11]
	v_cndmask_b32_e32 v14, v14, v38, vcc
	v_bitop3_b32 v32, v30, 64, v27 bitop3:0xc8
	v_cndmask_b32_e64 v15, v15, 5, vcc
	v_cmp_eq_u32_e32 vcc, 0, v32
	v_cmp_gt_f32_e64 s[10:11], v10, v14
	s_and_b64 vcc, vcc, s[10:11]
; __global__ void __launch_bounds__(512, 2) fwd_kernel(Params p) {
;     ...
;                 for (int k = 0; k < 4; ++k) { float best = -__builtin_inff(); int be = 0;
; #pragma unroll
;                     for (int e = 0; e < NE; ++e) { const bool take = !((mask >> e) & 1u) && lgv[e] > best; best = take ? lgv[e] : best; be = take ? e : be; }
;                     mask |= 1u << be; tv[k] = best; te[k] = be; }
;                 float ex[4], sum = 0.f;
; #pragma unroll
;                 for (int k = 0; k < 4; ++k) { ex[k] = __expf(tv[k] - tv[0]); sum += ex[k]; }
;                 const float inv = 1.0f / sum;
; #pragma unroll
;                 for (int k = 0; k < 4; ++k) { lrk[tid * 4 + k] = atomicAdd((int*)&hist[te[k]], 1); tok_e[tok * 4 + k] = te[k]; tok_w[tok * 4 + k] = ex[k] * inv; }
	v_cndmask_b32_e32 v10, v14, v10, vcc
	v_bitop3_b32 v14, v30, s0, v27 bitop3:0xc8
	v_cndmask_b32_e64 v15, v15, 6, vcc
	v_cmp_eq_u32_e32 vcc, 0, v14
	v_cmp_gt_f32_e64 s[10:11], v11, v10
	s_and_b64 vcc, vcc, s[10:11]
	s_movk_i32 s0, 0x100
	v_cndmask_b32_e32 v10, v10, v11, vcc
	v_bitop3_b32 v11, v30, s0, v27 bitop3:0xc8
	v_cndmask_b32_e64 v14, v15, 7, vcc
	v_cmp_eq_u32_e32 vcc, 0, v11
	v_cmp_gt_f32_e64 s[10:11], v41, v10
	s_and_b64 vcc, vcc, s[10:11]
	s_movk_i32 s0, 0x200
	v_cndmask_b32_e64 v11, v14, 8, vcc
	v_cndmask_b32_e32 v10, v10, v41, vcc
	v_bitop3_b32 v14, v30, s0, v27 bitop3:0xc8
	v_cmp_eq_u32_e32 vcc, 0, v14
	v_cmp_gt_f32_e64 s[10:11], v40, v10
	s_and_b64 vcc, vcc, s[10:11]
	s_movk_i32 s0, 0x400
	v_cndmask_b32_e32 v10, v10, v40, vcc
	v_bitop3_b32 v14, v30, s0, v27 bitop3:0xc8
	v_cndmask_b32_e64 v11, v11, 9, vcc
	v_cmp_eq_u32_e32 vcc, 0, v14
	v_cmp_gt_f32_e64 s[10:11], v6, v10
	s_and_b64 vcc, vcc, s[10:11]
	v_cndmask_b32_e32 v6, v10, v6, vcc
	v_bitop3_b32 v10, v30, s59, v27 bitop3:0xc8
	v_cndmask_b32_e64 v11, v11, 10, vcc
	v_cmp_eq_u32_e32 vcc, 0, v10
	v_cmp_gt_f32_e64 s[10:11], v7, v6
	s_and_b64 vcc, vcc, s[10:11]
	v_cndmask_b32_e32 v6, v6, v7, vcc
	v_bitop3_b32 v7, v30, s60, v27 bitop3:0xc8
	v_cndmask_b32_e64 v10, v11, 11, vcc
	v_cmp_eq_u32_e32 vcc, 0, v7
	v_cmp_gt_f32_e64 s[10:11], v43, v6
	s_and_b64 vcc, vcc, s[10:11]
	v_cndmask_b32_e64 v7, v10, 12, vcc
	v_cndmask_b32_e32 v6, v6, v43, vcc
	v_bitop3_b32 v10, v30, s61, v27 bitop3:0xc8
	v_cmp_eq_u32_e32 vcc, 0, v10
	v_cmp_gt_f32_e64 s[10:11], v42, v6
	s_and_b64 vcc, vcc, s[10:11]
	s_movk_i32 s0, 0x4000
	v_cndmask_b32_e32 v6, v6, v42, vcc
	v_bitop3_b32 v10, v30, s0, v27 bitop3:0xc8
	v_cndmask_b32_e64 v7, v7, 13, vcc
	v_cmp_eq_u32_e32 vcc, 0, v10
	v_cmp_gt_f32_e64 s[10:11], v2, v6
	s_and_b64 vcc, vcc, s[10:11]
	v_cndmask_b32_e32 v2, v6, v2, vcc
	v_bitop3_b32 v6, v30, s62, v27 bitop3:0xc8
	v_cndmask_b32_e64 v7, v7, 14, vcc
	v_cmp_eq_u32_e32 vcc, 0, v6
	v_cmp_gt_f32_e64 s[10:11], v3, v2
	s_and_b64 vcc, vcc, s[10:11]
	v_cndmask_b32_e32 v2, v2, v3, vcc
	v_bitop3_b32 v3, v30, s63, v27 bitop3:0xc8
	v_cndmask_b32_e64 v6, v7, 15, vcc
	v_cmp_eq_u32_e32 vcc, 0, v3
	v_cmp_gt_f32_e64 s[10:11], v4, v2
	s_and_b64 vcc, vcc, s[10:11]
	v_cndmask_b32_e32 v2, v2, v4, vcc
	v_bitop3_b32 v4, v30, s64, v27 bitop3:0xc8
	v_cndmask_b32_e64 v3, v6, 16, vcc
	v_cmp_eq_u32_e32 vcc, 0, v4
	v_cmp_gt_f32_e64 s[10:11], v0, v2
	s_and_b64 vcc, vcc, s[10:11]
	v_cndmask_b32_e32 v0, v2, v0, vcc
	v_bitop3_b32 v2, v30, s65, v27 bitop3:0xc8
	v_cndmask_b32_e64 v3, v3, 17, vcc
	v_cmp_eq_u32_e32 vcc, 0, v2
	v_cmp_gt_f32_e64 s[10:11], v1, v0
	s_and_b64 vcc, vcc, s[10:11]
	v_cndmask_b32_e32 v0, v0, v1, vcc
	v_bitop3_b32 v1, v30, s66, v27 bitop3:0xc8
	v_cndmask_b32_e64 v2, v3, 18, vcc
	v_cmp_eq_u32_e32 vcc, 0, v1
	v_cmp_gt_f32_e64 s[10:11], v33, v0
	s_and_b64 vcc, vcc, s[10:11]
	v_cndmask_b32_e64 v1, v2, 19, vcc
	v_cndmask_b32_e32 v0, v0, v33, vcc
	v_bitop3_b32 v2, v30, s67, v27 bitop3:0xc8
	v_cmp_eq_u32_e32 vcc, 0, v2
	v_cmp_gt_f32_e64 s[10:11], v8, v0
	s_and_b64 vcc, vcc, s[10:11]
	v_cndmask_b32_e32 v0, v0, v8, vcc
	v_bitop3_b32 v2, v30, s68, v27 bitop3:0xc8
	v_cndmask_b32_e64 v1, v1, 20, vcc
	v_cmp_eq_u32_e32 vcc, 0, v2
	v_cmp_gt_f32_e64 s[10:11], v5, v0
	s_and_b64 vcc, vcc, s[10:11]
	v_cndmask_b32_e32 v0, v0, v5, vcc
	v_bitop3_b32 v2, v30, s69, v27 bitop3:0xc8
	v_cndmask_b32_e64 v1, v1, 21, vcc
	v_cmp_eq_u32_e32 vcc, 0, v2
	v_cmp_gt_f32_e64 s[10:11], v9, v0
	s_and_b64 vcc, vcc, s[10:11]
	v_cndmask_b32_e32 v0, v0, v9, vcc
	v_bitop3_b32 v2, v30, s57, v27 bitop3:0xc8
	v_cndmask_b32_e64 v1, v1, 22, vcc
	v_cmp_eq_u32_e32 vcc, 0, v2
	v_cmp_gt_f32_e64 s[10:11], v29, v0
	s_and_b64 vcc, vcc, s[10:11]
	v_cndmask_b32_e32 v0, v0, v29, vcc
	v_bitop3_b32 v2, v30, s70, v27 bitop3:0xc8
	v_cndmask_b32_e64 v1, v1, 23, vcc
	v_cmp_eq_u32_e32 vcc, 0, v2
	v_cmp_gt_f32_e64 s[10:11], v13, v0
	s_and_b64 vcc, vcc, s[10:11]
	v_cndmask_b32_e32 v0, v0, v13, vcc
	v_bitop3_b32 v2, v30, s71, v27 bitop3:0xc8
	v_cndmask_b32_e64 v1, v1, 24, vcc
	v_cmp_eq_u32_e32 vcc, 0, v2
	v_cmp_gt_f32_e64 s[10:11], v12, v0
	s_and_b64 vcc, vcc, s[10:11]
	v_cndmask_b32_e32 v0, v0, v12, vcc
	v_bitop3_b32 v2, v30, s72, v27 bitop3:0xc8
	v_cndmask_b32_e64 v1, v1, 25, vcc
	v_cmp_eq_u32_e32 vcc, 0, v2
	v_cmp_gt_f32_e64 s[10:11], v22, v0
	s_and_b64 vcc, vcc, s[10:11]
	v_cndmask_b32_e32 v0, v0, v22, vcc
	v_bitop3_b32 v2, v30, s73, v27 bitop3:0xc8
	v_cndmask_b32_e64 v1, v1, 26, vcc
	v_cmp_eq_u32_e32 vcc, 0, v2
	v_cmp_gt_f32_e64 s[10:11], v25, v0
	s_and_b64 vcc, vcc, s[10:11]
	v_cndmask_b32_e32 v0, v0, v25, vcc
	v_bitop3_b32 v2, v30, s74, v27 bitop3:0xc8
	v_cndmask_b32_e64 v1, v1, 27, vcc
	v_cmp_eq_u32_e32 vcc, 0, v2
	v_cmp_gt_f32_e64 s[10:11], v23, v0
	s_and_b64 vcc, vcc, s[10:11]
	v_cndmask_b32_e32 v0, v0, v23, vcc
	v_bitop3_b32 v2, v30, s75, v27 bitop3:0xc8
	v_cndmask_b32_e64 v1, v1, 28, vcc
	v_cmp_eq_u32_e32 vcc, 0, v2
	v_cmp_gt_f32_e64 s[10:11], v19, v0
	s_and_b64 vcc, vcc, s[10:11]
	v_cndmask_b32_e32 v0, v0, v19, vcc
	v_bitop3_b32 v2, v30, 2.0, v27 bitop3:0xc8
	v_cndmask_b32_e64 v1, v1, 29, vcc
	v_cmp_eq_u32_e32 vcc, 0, v2
	v_cmp_gt_f32_e64 s[10:11], v20, v0
	s_and_b64 vcc, vcc, s[10:11]
	v_cndmask_b32_e32 v0, v0, v20, vcc
	v_cndmask_b32_e64 v1, v1, 30, vcc
	v_cmp_lt_i32_e32 vcc, -1, v31
	v_cmp_gt_f32_e64 s[10:11], v21, v0
	s_and_b64 vcc, vcc, s[10:11]
	v_cndmask_b32_e64 v19, v1, 31, vcc
	v_sub_f32_e32 v1, v24, v24
	v_sub_f32_e32 v2, v26, v24
	v_mul_f32_e32 v1, 0x3fb8aa3b, v1
	v_mul_f32_e32 v2, 0x3fb8aa3b, v2
	v_cndmask_b32_e32 v0, v0, v21, vcc
	v_exp_f32_e32 v6, v1
	v_exp_f32_e32 v7, v2
	v_sub_f32_e32 v2, v28, v24
	v_mul_f32_e32 v2, 0x3fb8aa3b, v2
	v_sub_f32_e32 v0, v0, v24
	v_exp_f32_e32 v8, v2
	v_mul_f32_e32 v0, 0x3fb8aa3b, v0
	v_exp_f32_e32 v9, v0
	v_add_f32_e32 v1, 0, v6
	v_add_f32_e32 v1, v1, v7
	v_add_f32_e32 v1, v1, v8
	v_add_f32_e32 v0, v1, v9
	v_div_scale_f32 v1, s[0:1], v0, v0, 1.0
	v_rcp_f32_e32 v2, v1
	v_add_u32_e32 v11, 0, v134
	v_fma_f32 v3, -v1, v2, 1.0
	v_fmac_f32_e32 v2, v3, v2
	v_div_scale_f32 v3, vcc, 1.0, v0, 1.0
	v_mul_f32_e32 v4, v3, v2
	v_fma_f32 v5, -v1, v4, v3
	v_fmac_f32_e32 v4, v5, v2
	v_fma_f32 v1, -v1, v4, v3
	v_div_fmas_f32 v1, v1, v2, v4
	v_div_fixup_f32 v10, v1, v0, 1.0
	v_lshl_add_u32 v1, v16, 2, 0
	ds_add_rtn_u32 v1, v1, v138 offset:53760
	v_lshlrev_b32_e32 v0, 2, v34
	s_waitcnt lgkmcnt(0)
; __global__ void __launch_bounds__(512, 2) fwd_kernel(Params p) {
;     ...
;                 float ex[4], sum = 0.f;
; #pragma unroll
;                 for (int k = 0; k < 4; ++k) { ex[k] = __expf(tv[k] - tv[0]); sum += ex[k]; }
;                 const float inv = 1.0f / sum;
; #pragma unroll
;                 for (int k = 0; k < 4; ++k) { lrk[tid * 4 + k] = atomicAdd((int*)&hist[te[k]], 1); tok_e[tok * 4 + k] = te[k]; tok_w[tok * 4 + k] = ex[k] * inv; }
	ds_write_b32 v11, v1 offset:40960
	v_ashrrev_i32_e32 v1, 31, v0
	v_lshlrev_b64 v[2:3], 2, v[0:1]
	v_lshl_add_u64 v[4:5], s[16:17], 0, v[2:3]
	v_mul_f32_e32 v1, v10, v6
	v_mov_b32_e32 v240, v1
	v_lshl_add_u64 v[2:3], s[42:43], 0, v[2:3]
	global_store_dword v[2:3], v1, off
	v_lshl_add_u32 v1, v17, 2, 0
	ds_add_rtn_u32 v1, v1, v138 offset:53760
	v_or_b32_e32 v2, 1, v0
	v_ashrrev_i32_e32 v3, 31, v2
	v_mul_f32_e32 v0, v10, v7
	v_lshl_add_u64 v[6:7], v[2:3], 2, s[42:43]
	s_waitcnt lgkmcnt(0)
	ds_write_b32 v11, v1 offset:40964
	v_lshl_add_u32 v1, v18, 2, 0
	ds_add_rtn_u32 v1, v1, v138 offset:53760
	v_lshl_add_u32 v2, v19, 2, 0
	s_waitcnt lgkmcnt(0)
	ds_write_b32 v11, v1 offset:40968
	ds_add_rtn_u32 v2, v2, v138 offset:53760
	v_mul_f32_e32 v1, v10, v8
	global_store_dwordx4 v[4:5], v[16:19], off
	s_waitcnt lgkmcnt(0)
	ds_write_b32 v11, v2 offset:40972
	v_mul_f32_e32 v2, v10, v9
	v_mov_b32_e32 v241, v0
	v_mov_b32_e32 v242, v1
	v_mov_b32_e32 v243, v2
	global_store_dwordx3 v[6:7], v[0:2], off

; __global__ void __launch_bounds__(512, 2) fwd_kernel(Params p) {
;     ...
;             __syncthreads();
;             if (tid < 32) base[tid] = (int)__hip_atomic_fetch_add(cnt + tid, (unsigned)hist[tid], RLX_AGENT);
;             __syncthreads();
;             if (tid < 64) { const int tok = blk * 64 + tid; const float rsv = RS2[tok];
; #pragma unroll
;                 for (int k = 0; k < 4; ++k) { const int rk = base[te[k]] + lrk[tid * 4 + k]; tok_rank[tok * 4 + k] = rk; lrk[tid * 4 + k] = te[k] * XCAP + rk;
;                     row_w[(size_t)te[k] * XCAP + rk] = tok_w[tok * 4 + k]; row_rs[(size_t)te[k] * XCAP + rk] = rsv; } }
.LBB0_988:
	s_or_b64 exec, exec, s[10:11]
	s_waitcnt lgkmcnt(0)
	s_barrier
	s_and_saveexec_b64 s[10:11], s[6:7]
	s_cbranch_execz .LBB0_990
	v_lshlrev_b32_e32 v6, 2, v34
	v_ashrrev_i32_e32 v7, 31, v6
	v_lshl_add_u64 v[0:1], v[34:35], 2, s[44:45]
	v_lshlrev_b64 v[8:9], 2, v[6:7]
	v_mov_b32_e32 v22, v244
	v_lshl_add_u64 v[0:1], s[42:43], 0, v[8:9]
	v_lshl_add_u32 v0, v16, 2, 0
	v_add_u32_e32 v23, 0, v134
	ds_read_b32 v20, v0 offset:54016
	ds_read_b128 v[0:3], v23 offset:40960
	v_ashrrev_i32_e32 v5, 31, v16
	v_mov_b32_e32 v4, v16
	v_lshlrev_b64 v[4:5], 16, v[4:5]
	v_lshl_add_u64 v[12:13], s[22:23], 0, v[4:5]
	v_lshl_add_u64 v[14:15], s[26:27], 0, v[4:5]
	s_waitcnt lgkmcnt(0)
	v_add_u32_e32 v4, v0, v20
	v_ashrrev_i32_e32 v5, 31, v4
	v_or_b32_e32 v10, 1, v6
	v_lshlrev_b64 v[20:21], 2, v[4:5]
	v_ashrrev_i32_e32 v11, 31, v10
	v_lshl_add_u64 v[14:15], v[14:15], 0, v[20:21]
	v_lshl_add_u64 v[10:11], v[10:11], 2, s[42:43]
	v_lshl_add_u64 v[12:13], v[12:13], 0, v[20:21]
	v_lshl_add_u32 v0, v17, 2, 0
	v_lshl_add_u64 v[8:9], s[18:19], 0, v[8:9]
	global_store_dword v[14:15], v22, off
	global_store_dword v[12:13], v240, off
	v_lshl_add_u32 v7, v16, 14, v4
	ds_write_b32 v23, v7 offset:40960
	ds_read_b32 v0, v0 offset:54016
	v_ashrrev_i32_e32 v11, 31, v17
	v_mov_b32_e32 v10, v17
	v_lshlrev_b64 v[10:11], 16, v[10:11]
	v_or_b32_e32 v12, 2, v6
	s_waitcnt lgkmcnt(0)
	v_add_u32_e32 v0, v1, v0
	v_ashrrev_i32_e32 v1, 31, v0
	v_lshl_add_u64 v[14:15], s[22:23], 0, v[10:11]
	v_lshl_add_u64 v[10:11], s[26:27], 0, v[10:11]
	v_lshlrev_b64 v[20:21], 2, v[0:1]
	v_ashrrev_i32_e32 v13, 31, v12
	v_lshl_add_u64 v[10:11], v[10:11], 0, v[20:21]
	v_lshl_add_u64 v[12:13], v[12:13], 2, s[42:43]
	v_lshl_add_u64 v[14:15], v[14:15], 0, v[20:21]
	v_lshl_add_u32 v7, v17, 14, v0
	v_or_b32_e32 v6, 3, v6
	global_store_dword v[10:11], v22, off
	global_store_dword v[14:15], v241, off
	v_lshl_add_u32 v5, v18, 2, 0
	ds_write_b32 v23, v7 offset:40964
	ds_read_b32 v5, v5 offset:54016
	v_ashrrev_i32_e32 v7, 31, v6
	v_ashrrev_i32_e32 v11, 31, v18
	v_mov_b32_e32 v10, v18
	v_lshl_add_u64 v[14:15], v[6:7], 2, s[42:43]
	s_waitcnt lgkmcnt(0)
	v_add_u32_e32 v6, v2, v5
	v_lshlrev_b64 v[10:11], 16, v[10:11]
	v_ashrrev_i32_e32 v7, 31, v6
	v_lshl_add_u64 v[12:13], s[22:23], 0, v[10:11]
	v_lshl_add_u64 v[10:11], s[26:27], 0, v[10:11]
	v_lshlrev_b64 v[20:21], 2, v[6:7]
	v_lshl_add_u64 v[10:11], v[10:11], 0, v[20:21]
	v_lshl_add_u64 v[12:13], v[12:13], 0, v[20:21]
	v_lshl_add_u32 v2, v18, 14, v6
	v_mov_b32_e32 v5, v0
	global_store_dword v[10:11], v22, off
	global_store_dword v[12:13], v242, off
	v_lshl_add_u32 v1, v19, 2, 0
	ds_write_b32 v23, v2 offset:40968
	ds_read_b32 v1, v1 offset:54016
	v_ashrrev_i32_e32 v11, 31, v19
	v_mov_b32_e32 v10, v19
	v_lshlrev_b64 v[10:11], 16, v[10:11]
	v_lshl_add_u64 v[12:13], s[22:23], 0, v[10:11]
	s_waitcnt lgkmcnt(0)
	v_add_u32_e32 v7, v3, v1
	v_ashrrev_i32_e32 v1, 31, v7
	v_mov_b32_e32 v0, v7
	v_lshl_add_u32 v2, v19, 14, v7
	v_lshlrev_b64 v[0:1], 2, v[0:1]
	v_lshl_add_u64 v[10:11], s[26:27], 0, v[10:11]
	ds_write_b32 v23, v2 offset:40972
	v_lshl_add_u64 v[2:3], v[12:13], 0, v[0:1]
	global_store_dwordx4 v[8:9], v[4:7], off
	v_lshl_add_u64 v[0:1], v[10:11], 0, v[0:1]
	global_store_dword v[2:3], v243, off
	global_store_dword v[0:1], v22, off

; #define LAS __attribute__((address_space(3)))
; __device__ __forceinline__ int lane_id() { int l; asm volatile("v_mbcnt_lo_u32_b32 %0, -1, 0\n\tv_mbcnt_hi_u32_b32 %0, -1, %0" : "=v"(l)); return l; }
; __device__ __forceinline__ int xcd_chunk(int L, int nwg) { const int q = nwg / NXCD, r = nwg % NXCD, xcd = L % NXCD, off = L / NXCD; return (xcd < r ? xcd * (q + 1) : r * (q + 1) + (xcd - r) * q) + off; }
; #define LANE_TID() const int lane = lane_id(), tid = wave * 64 + lane
;     __device__ __forceinline__ void init(const void* A_, int slabA_, const void* Bt_, size_t estride_bytes, int rowbytes, const LAS int* ts_, int nN_, int G_, int c_) { slabA = slabA_; A = (const char*)A_; Bt = (const char*)Bt_; estride = estride_bytes; rowb = rowbytes; ts = ts_; nN = nN_; nwg = __b ...
;     __device__ __forceinline__ bool next(int i, Unit& u) const {
;         const int L = i * G + c; if (L >= nwg) return false;
;         const int wgid = xcd_chunk(L, nwg);
;         const int lj = lane_id() & 31;
;         const unsigned long long bal = __ballot(ts[lj] * nN <= wgid);
;         const int e = __builtin_popcount((unsigned)bal) - 1;
;         const int t0 = __builtin_amdgcn_readfirstlane(ts[e]), mt = __builtin_amdgcn_readfirstlane(ts[e + 1]) - t0, uu = wgid - t0 * nN;
;         const int lt = uu % mt; u.pm = t0 + lt; u.pn = uu / mt; u.e = e; u.lr0 = lt * BM;
;         u.A = A + (slabA ? ((size_t)e * XCAP + (size_t)lt * BM) : (size_t)u.pm * BM) * rowb; u.B = Bt + (size_t)e * estride + (size_t)u.pn * BM * rowb; return true;
; __global__ void __launch_bounds__(512, 2) fwd_kernel(Params p) {
;     ...
;     if (IN(11)) { LANE_TID();
;         moe_tables(ctl + CW_CNT, ts, tid);
;         pg8::MoeOrder S; S.init(ACT, 0, WdT, (size_t)DM * DFF, DFF, ts, 8, G, bx);
;         pg8::EpiDown E{Yb, p.in[I_BD], row_w};
.LBB0_1120:
	s_or_b64 exec, exec, s[6:7]
	s_waitcnt lgkmcnt(0)
	s_barrier
	v_mbcnt_lo_u32_b32 v0, -1, 0
	v_mbcnt_hi_u32_b32 v0, -1, v0
	v_readlane_b32 s0, v252, 3
	s_nop 1
	v_add_u32_e32 v0, s0, v0
	s_add_u32 s6, s28, 0x8a000000
	s_addc_u32 s7, s29, 0
	s_add_i32 s0, 0, 0x25180
	v_mov_b32_e32 v0, s0
	s_waitcnt lgkmcnt(0)
	s_barrier
	ds_read_b32 v0, v0
	s_waitcnt lgkmcnt(0)
	v_readfirstlane_b32 s0, v0
	s_lshl_b32 s1, s0, 3
	s_cmp_ge_i32 s2, s1
	v_mbcnt_lo_u32_b32 v0, -1, 0
	v_mbcnt_hi_u32_b32 v0, -1, v0
	s_cbranch_scc1 .LBB0_1140
	v_lshl_add_u32 v1, v0, 4, s35
	v_ashrrev_i32_e32 v2, 31, v1
	v_lshrrev_b32_e32 v2, 22, v2
	v_add_u32_e32 v2, v1, v2
	v_ashrrev_i32_e32 v2, 10, v2
	v_mul_i32_i24_e32 v3, 0x400, v2
	v_sub_u32_e32 v3, v1, v3
	v_lshrrev_b32_e32 v4, 4, v3
	v_bitop3_b32 v3, v4, v3, 32 bitop3:0x6c
	v_ashrrev_i32_e32 v5, 31, v3
	v_lshrrev_b32_e32 v5, 26, v5
	v_lshlrev_b32_e32 v4, 3, v2
	v_add_u32_e32 v5, v3, v5
	v_and_b32_e32 v4, -16, v4
	v_ashrrev_i32_e32 v6, 6, v5
	v_and_b32_e32 v5, 0xc0, v5
	v_add_u32_e32 v4, v6, v4
	v_sub_u32_e32 v3, v3, v5
	v_mov_b32_e32 v5, 1
	v_lshlrev_b32_e32 v2, 5, v2
	v_ashrrev_i16_sdwa v3, v5, sext(v3) dst_sel:DWORD dst_unused:UNUSED_PAD src0_sel:DWORD src1_sel:BYTE_0
	v_lshlrev_b32_e32 v7, 1, v4
	s_waitcnt vmcnt(16)
	v_lshrrev_b32_e32 v8, 2, v4
	v_and_b32_e32 v6, 3, v6
	s_mov_b32 s9, 0x1fffe0
	v_and_b32_e32 v2, 32, v2
	v_bfe_i32 v3, v3, 0, 16
	v_and_b32_e32 v7, 24, v7
	v_and_b32_e32 v8, 4, v8
	v_and_or_b32 v6, v4, s9, v6
	v_or3_b32 v6, v6, v8, v7
	v_add_lshl_u32 v2, v2, v3, 1
	v_add_u32_e32 v1, 0x2000, v1
	v_lshl_add_u32 v152, v4, 11, v2
	v_lshl_add_u32 v153, v6, 11, v2
	v_ashrrev_i32_e32 v2, 31, v1
	v_lshrrev_b32_e32 v2, 22, v2
	v_add_u32_e32 v2, v1, v2
	v_ashrrev_i32_e32 v2, 10, v2
	v_mul_i32_i24_e32 v3, 0x400, v2
	v_sub_u32_e32 v1, v1, v3
	v_lshrrev_b32_e32 v3, 4, v1
	v_bitop3_b32 v1, v3, v1, 32 bitop3:0x6c
	s_ashr_i32 s3, s2, 31
	v_ashrrev_i32_e32 v4, 31, v1
	s_lshr_b32 s3, s3, 29
	v_lshrrev_b32_e32 v4, 26, v4
	s_add_i32 s3, s2, s3
	v_lshlrev_b32_e32 v3, 3, v2
	v_add_u32_e32 v4, v1, v4
	s_ashr_i32 s12, s3, 3
	s_and_b32 s3, s3, -8
	v_and_b32_e32 v3, -16, v3
	v_ashrrev_i32_e32 v6, 6, v4
	s_sub_i32 s13, s2, s3
	s_add_i32 s3, s0, 1
	s_load_dwordx2 s[10:11], s[88:89], 0xa8
	v_add_u32_e32 v7, v6, v3
	s_cmp_lt_i32 s13, 0
	v_mbcnt_lo_u32_b32 v3, -1, 0
	v_mbcnt_hi_u32_b32 v3, -1, v3
	v_lshlrev_b32_e32 v2, 5, v2
	s_cselect_b32 s24, s3, s0
	v_and_b32_e32 v3, 31, v3
	s_add_i32 s8, 0, 0x25100
	v_and_b32_e32 v8, 32, v2
	v_and_b32_e32 v2, 0xffc0, v4
	v_lshl_add_u32 v3, v3, 2, s8
	v_sub_u32_e32 v1, v1, v2
	ds_read_b32 v3, v3
	v_lshrrev_b16_e32 v2, 7, v1
	v_and_b32_e32 v2, 1, v2
	v_add_u16_e32 v1, v1, v2
	v_lshlrev_b32_e32 v2, 1, v7
	v_and_b32_e32 v4, 24, v2
	v_lshrrev_b32_e32 v2, 2, v7
	s_mul_i32 s13, s24, s13
	v_ashrrev_i16_sdwa v1, v5, sext(v1) dst_sel:DWORD dst_unused:UNUSED_PAD src0_sel:DWORD src1_sel:BYTE_0
	v_and_b32_e32 v5, 4, v2
	s_add_i32 s13, s13, s12
	s_waitcnt lgkmcnt(0)
	v_lshlrev_b32_e32 v2, 3, v3
	v_cmp_ge_i32_e32 vcc, s13, v2
	s_bcnt1_i32_b32 s12, vcc_lo
	s_add_i32 s56, s12, -1
	s_lshl_b32 s12, s56, 2
	s_add_i32 s12, s8, s12
	v_mov_b32_e32 v2, s12
	ds_read2_b32 v[2:3], v2 offset1:1
	v_and_b32_e32 v6, 3, v6
	v_and_or_b32 v6, v7, s9, v6
	v_bfe_i32 v1, v1, 0, 16
	v_or3_b32 v4, v6, v5, v4
	s_waitcnt lgkmcnt(0)
	v_readfirstlane_b32 s12, v2
	v_readfirstlane_b32 s9, v3
	s_sub_i32 s24, s9, s12
	s_abs_i32 s25, s24
	v_cvt_f32_u32_e32 v2, s25
	v_add_lshl_u32 v1, v8, v1, 1
	v_lshl_add_u32 v154, v7, 11, v1
	v_lshl_add_u32 v155, v4, 11, v1
	v_rcp_iflag_f32_e32 v1, v2
	s_sub_i32 s30, 0, s25
	s_lshl_b32 s26, s12, 3
	s_sub_i32 s13, s13, s26
	v_mul_f32_e32 v1, 0x4f7ffffe, v1
	v_cvt_u32_f32_e32 v1, v1
	s_abs_i32 s27, s13
	s_xor_b32 s26, s13, s24
	s_ashr_i32 s57, s56, 31
	v_readfirstlane_b32 s31, v1
	s_mul_i32 s30, s30, s31
	s_mul_hi_u32 s30, s31, s30
	s_add_i32 s31, s31, s30
	s_mul_hi_u32 s30, s27, s31
	s_mul_i32 s31, s30, s25
	s_sub_i32 s27, s27, s31
	s_ashr_i32 s26, s26, 31
	s_add_i32 s31, s30, 1
	s_sub_i32 s35, s27, s25
	s_cmp_ge_u32 s27, s25
	s_cselect_b32 s30, s31, s30
	s_cselect_b32 s27, s35, s27
	s_add_i32 s31, s30, 1
	s_cmp_ge_u32 s27, s25
	s_cselect_b32 s25, s31, s30
	s_xor_b32 s25, s25, s26
	s_sub_i32 s58, s25, s26
	s_mul_i32 s24, s58, s24
	s_sub_i32 s26, s13, s24
	s_add_i32 s60, s26, s12
	s_ashr_i32 s61, s60, 31
	s_lshl_b64 s[12:13], s[60:61], 19
	s_add_u32 s64, s4, s12
	s_addc_u32 s65, s5, s13
	s_lshl_b64 s[12:13], s[56:57], 22
	s_add_u32 s24, s77, s12
	v_readlane_b32 s12, v252, 33
	s_addc_u32 s25, s12, s13
	s_ashr_i32 s59, s58, 31
	s_lshl_b64 s[12:13], s[58:59], 19
	s_add_u32 s66, s24, s12
	s_addc_u32 s67, s25, s13
	s_add_i32 s30, s97, 0x10000
	s_mov_b32 s12, m0
	s_mov_b32 m0, s30
	s_nop 0
	global_load_lds_dwordx4 v153, s[66:67]
	s_mov_b32 m0, s12
	s_add_i32 s31, s97, 0x12000
	s_mov_b32 s12, m0
	s_mov_b32 m0, s31
	s_nop 0
	global_load_lds_dwordx4 v155, s[66:67]
	s_mov_b32 m0, s12
	s_add_u32 s24, s66, 0x40000
	s_addc_u32 s25, s67, 0
	s_add_i32 s37, s97, 0x14000
	s_mov_b32 s27, m0
	s_mov_b32 m0, s37
	s_nop 0
	global_load_lds_dwordx4 v153, s[24:25]
	s_mov_b32 m0, s27
	s_add_i32 s59, s97, 0x16000
	s_mov_b32 s27, m0
	s_mov_b32 m0, s59
	s_nop 0
	global_load_lds_dwordx4 v155, s[24:25]
	s_mov_b32 m0, s27
	s_add_i32 s61, s97, 0x2000
	s_mov_b32 s24, m0
	s_mov_b32 m0, s97
	s_nop 0
	global_load_lds_dwordx4 v152, s[64:65]
	s_mov_b32 m0, s24
	s_add_u32 s38, s64, 0x40000
	s_mov_b32 s24, m0
	s_mov_b32 m0, s61
	s_nop 0
	global_load_lds_dwordx4 v154, s[64:65]
	s_mov_b32 m0, s24
	s_addc_u32 s39, s65, 0
	s_add_i32 s74, s97, 0x4000
	s_add_i32 s75, s97, 0x6000
	v_readlane_b32 s27, v252, 10
	s_mov_b32 s24, m0
	s_mov_b32 m0, s74
	s_nop 0
	global_load_lds_dwordx4 v152, s[38:39]
	s_mov_b32 m0, s24
	s_cmp_eq_u32 s27, 1
	s_cselect_b64 s[24:25], -1, 0
	s_cmp_lg_u32 s27, 1
	s_mov_b32 s27, m0
	s_mov_b32 m0, s75
	s_nop 0
	global_load_lds_dwordx4 v154, s[38:39]
	s_mov_b32 m0, s27
	s_mov_b32 s9, 0
	s_mov_b64 s[12:13], 0x40000
	s_cbranch_scc1 .LBB0_1127
	s_barrier

; #define LANE_TID() const int lane = lane_id(), tid = wave * 64 + lane
; __global__ void __launch_bounds__(512, 2) fwd_kernel(Params p) {
;     ...
;     if (IN(12)) { LANE_TID();
;         moe_tables(ctl + CW_CNT, ts, tid);
;         constexpr int NI = T * (DM / 16), UN = 4;
;         for (int it0 = GT(); it0 < NI; it0 += UN * NGT) {
;             int mm[UN], cc[UN], ee[UN][4], rk[UN][4]; u32x4 xa[UN], xb[UN], y[UN][4];
; #pragma unroll
;             for (int u = 0; u < UN; ++u) { const int it = it0 + u * NGT < NI ? it0 + u * NGT : it0; mm[u] = it >> 7; cc[u] = (it & 127) * 16;
.LBB0_1194:
	s_or_b64 exec, exec, s[2:3]
	s_waitcnt lgkmcnt(0)
	s_barrier
	v_mbcnt_lo_u32_b32 v0, -1, 0
	v_mbcnt_hi_u32_b32 v0, -1, v0
	v_readlane_b32 s0, v252, 3
	s_nop 1
	v_add_u32_e32 v0, s0, v0
	v_readlane_b32 s0, v252, 7
	s_mov_b32 s11, 0x200000
	s_waitcnt vmcnt(9) lgkmcnt(0)
	v_add_u32_e32 v88, s0, v0
	v_cmp_gt_i32_e32 vcc, s11, v88
	s_barrier
	s_and_saveexec_b64 s[0:1], vcc
	s_cbranch_execz .LBB0_1207
	s_load_dwordx2 s[4:5], s[88:89], 0xb0
	s_lshl_b32 s20, s33, 11
	v_lshlrev_b32_e32 v89, 4, v88
	s_lshl_b32 s21, s33, 15
	s_lshl_b32 s22, s33, 10
	s_mulk_i32 s33, 0x600
	s_mov_b64 s[8:9], 0
	s_waitcnt vmcnt(5)
	v_mov_b32_e32 v73, 0
	s_add_i32 s23, 0, 0x25100
	s_mov_b32 s10, 0x3d800000
	s_mov_b32 s24, 0x1fffff
	s_branch .LBB0_1201
